# attention P.V: the V-fragment LDS reads of the next column block interleaved two per MFMA (counted lgkmcnt per MFMA) instead of a burst of eight behind each dependent MFMA group
# speedup vs baseline: 1.0099x; 1.0057x over previous
.LBB0_520:
	ds_read_b64_tr_b16 v[144:145], v177 offset:0
	ds_read_b64_tr_b16 v[146:147], v177 offset:0x1000
	ds_read_b64_tr_b16 v[148:149], v177 offset:0x2000
	ds_read_b64_tr_b16 v[150:151], v177 offset:0x3000
	ds_read_b64_tr_b16 v[152:153], v177 offset:0x4000
	ds_read_b64_tr_b16 v[154:155], v177 offset:0x5000
	ds_read_b64_tr_b16 v[156:157], v177 offset:0x6000
	ds_read_b64_tr_b16 v[158:159], v177 offset:0x7000
	s_waitcnt lgkmcnt(6)
	s_nop 0
	v_mfma_f32_32x32x16_bf16 v[112:127], v[144:147], v[128:131], v[112:127]
	ds_read_b64_tr_b16 v[198:199], v177 offset:0x200
	ds_read_b64_tr_b16 v[200:201], v177 offset:0x1200
	s_waitcnt lgkmcnt(6)
	v_mfma_f32_32x32x16_bf16 v[112:127], v[148:151], v[132:135], v[112:127]
	ds_read_b64_tr_b16 v[202:203], v177 offset:0x2200
	ds_read_b64_tr_b16 v[204:205], v177 offset:0x3200
	s_waitcnt lgkmcnt(6)
	v_mfma_f32_32x32x16_bf16 v[112:127], v[152:155], v[136:139], v[112:127]
	ds_read_b64_tr_b16 v[206:207], v177 offset:0x4200
	ds_read_b64_tr_b16 v[208:209], v177 offset:0x5200
	s_waitcnt lgkmcnt(6)
	v_mfma_f32_32x32x16_bf16 v[112:127], v[156:159], v[140:143], v[112:127]
	ds_read_b64_tr_b16 v[210:211], v177 offset:0x6200
	ds_read_b64_tr_b16 v[212:213], v177 offset:0x7200
	s_waitcnt lgkmcnt(6)
	v_mfma_f32_32x32x16_bf16 v[0:15], v[198:201], v[128:131], v[0:15]
	ds_read_b64_tr_b16 v[144:145], v177 offset:0x400
	ds_read_b64_tr_b16 v[146:147], v177 offset:0x1400
	s_waitcnt lgkmcnt(6)
	v_mfma_f32_32x32x16_bf16 v[0:15], v[202:205], v[132:135], v[0:15]
	ds_read_b64_tr_b16 v[148:149], v177 offset:0x2400
	ds_read_b64_tr_b16 v[150:151], v177 offset:0x3400
	s_waitcnt lgkmcnt(6)
	v_mfma_f32_32x32x16_bf16 v[0:15], v[206:209], v[136:139], v[0:15]
	ds_read_b64_tr_b16 v[152:153], v177 offset:0x4400
	ds_read_b64_tr_b16 v[154:155], v177 offset:0x5400
	s_waitcnt lgkmcnt(6)
	v_mfma_f32_32x32x16_bf16 v[0:15], v[210:213], v[140:143], v[0:15]
	ds_read_b64_tr_b16 v[156:157], v177 offset:0x6400
	ds_read_b64_tr_b16 v[158:159], v177 offset:0x7400
	s_waitcnt lgkmcnt(6)
	v_mfma_f32_32x32x16_bf16 v[16:31], v[144:147], v[128:131], v[16:31]
	ds_read_b64_tr_b16 v[198:199], v177 offset:0x600
	ds_read_b64_tr_b16 v[200:201], v177 offset:0x1600
	s_waitcnt lgkmcnt(6)
	v_mfma_f32_32x32x16_bf16 v[16:31], v[148:151], v[132:135], v[16:31]
	ds_read_b64_tr_b16 v[202:203], v177 offset:0x2600
	ds_read_b64_tr_b16 v[204:205], v177 offset:0x3600
	s_waitcnt lgkmcnt(6)
	v_mfma_f32_32x32x16_bf16 v[16:31], v[152:155], v[136:139], v[16:31]
	ds_read_b64_tr_b16 v[206:207], v177 offset:0x4600
	ds_read_b64_tr_b16 v[208:209], v177 offset:0x5600
	s_waitcnt lgkmcnt(6)
	v_mfma_f32_32x32x16_bf16 v[16:31], v[156:159], v[140:143], v[16:31]
	ds_read_b64_tr_b16 v[210:211], v177 offset:0x6600
	ds_read_b64_tr_b16 v[212:213], v177 offset:0x7600
	s_waitcnt lgkmcnt(6)
	v_mfma_f32_32x32x16_bf16 v[32:47], v[198:201], v[128:131], v[32:47]
	ds_read_b64_tr_b16 v[144:145], v177 offset:0x800
	ds_read_b64_tr_b16 v[146:147], v177 offset:0x1800
	s_waitcnt lgkmcnt(6)
	v_mfma_f32_32x32x16_bf16 v[32:47], v[202:205], v[132:135], v[32:47]
	ds_read_b64_tr_b16 v[148:149], v177 offset:0x2800
	ds_read_b64_tr_b16 v[150:151], v177 offset:0x3800
	s_waitcnt lgkmcnt(6)
	v_mfma_f32_32x32x16_bf16 v[32:47], v[206:209], v[136:139], v[32:47]
	ds_read_b64_tr_b16 v[152:153], v177 offset:0x4800
	ds_read_b64_tr_b16 v[154:155], v177 offset:0x5800
	s_waitcnt lgkmcnt(6)
	v_mfma_f32_32x32x16_bf16 v[32:47], v[210:213], v[140:143], v[32:47]
	ds_read_b64_tr_b16 v[156:157], v177 offset:0x6800
	ds_read_b64_tr_b16 v[158:159], v177 offset:0x7800
	s_waitcnt lgkmcnt(6)
	v_mfma_f32_32x32x16_bf16 v[48:63], v[144:147], v[128:131], v[48:63]
	ds_read_b64_tr_b16 v[198:199], v177 offset:0xa00
	ds_read_b64_tr_b16 v[200:201], v177 offset:0x1a00
	s_waitcnt lgkmcnt(6)
	v_mfma_f32_32x32x16_bf16 v[48:63], v[148:151], v[132:135], v[48:63]
	ds_read_b64_tr_b16 v[202:203], v177 offset:0x2a00
	ds_read_b64_tr_b16 v[204:205], v177 offset:0x3a00
	s_waitcnt lgkmcnt(6)
	v_mfma_f32_32x32x16_bf16 v[48:63], v[152:155], v[136:139], v[48:63]
	ds_read_b64_tr_b16 v[206:207], v177 offset:0x4a00
	ds_read_b64_tr_b16 v[208:209], v177 offset:0x5a00
	s_waitcnt lgkmcnt(6)
	v_mfma_f32_32x32x16_bf16 v[48:63], v[156:159], v[140:143], v[48:63]
	ds_read_b64_tr_b16 v[210:211], v177 offset:0x6a00
	ds_read_b64_tr_b16 v[212:213], v177 offset:0x7a00
	s_waitcnt lgkmcnt(6)
	v_mfma_f32_32x32x16_bf16 v[64:79], v[198:201], v[128:131], v[64:79]
	ds_read_b64_tr_b16 v[144:145], v177 offset:0xc00
	ds_read_b64_tr_b16 v[146:147], v177 offset:0x1c00
	s_waitcnt lgkmcnt(6)
	v_mfma_f32_32x32x16_bf16 v[64:79], v[202:205], v[132:135], v[64:79]
	ds_read_b64_tr_b16 v[148:149], v177 offset:0x2c00
	ds_read_b64_tr_b16 v[150:151], v177 offset:0x3c00
	s_waitcnt lgkmcnt(6)
	v_mfma_f32_32x32x16_bf16 v[64:79], v[206:209], v[136:139], v[64:79]
	ds_read_b64_tr_b16 v[152:153], v177 offset:0x4c00
	ds_read_b64_tr_b16 v[154:155], v177 offset:0x5c00
	s_waitcnt lgkmcnt(6)
	v_mfma_f32_32x32x16_bf16 v[64:79], v[210:213], v[140:143], v[64:79]
	ds_read_b64_tr_b16 v[156:157], v177 offset:0x6c00
	ds_read_b64_tr_b16 v[158:159], v177 offset:0x7c00
	s_waitcnt lgkmcnt(6)
	v_mfma_f32_32x32x16_bf16 v[80:95], v[144:147], v[128:131], v[80:95]
	ds_read_b64_tr_b16 v[198:199], v177 offset:0xe00
	ds_read_b64_tr_b16 v[200:201], v177 offset:0x1e00
	s_waitcnt lgkmcnt(6)
	v_mfma_f32_32x32x16_bf16 v[80:95], v[148:151], v[132:135], v[80:95]
	ds_read_b64_tr_b16 v[202:203], v177 offset:0x2e00
	ds_read_b64_tr_b16 v[204:205], v177 offset:0x3e00
	s_waitcnt lgkmcnt(6)
	v_mfma_f32_32x32x16_bf16 v[80:95], v[152:155], v[136:139], v[80:95]
	ds_read_b64_tr_b16 v[206:207], v177 offset:0x4e00
	ds_read_b64_tr_b16 v[208:209], v177 offset:0x5e00
	s_waitcnt lgkmcnt(6)
	v_mfma_f32_32x32x16_bf16 v[80:95], v[156:159], v[140:143], v[80:95]
	ds_read_b64_tr_b16 v[210:211], v177 offset:0x6e00
	ds_read_b64_tr_b16 v[212:213], v177 offset:0x7e00
	s_waitcnt lgkmcnt(6)
	v_mfma_f32_32x32x16_bf16 v[96:111], v[198:201], v[128:131], v[96:111]
	s_waitcnt lgkmcnt(4)
	v_mfma_f32_32x32x16_bf16 v[96:111], v[202:205], v[132:135], v[96:111]
	s_waitcnt lgkmcnt(2)
	v_mfma_f32_32x32x16_bf16 v[96:111], v[206:209], v[136:139], v[96:111]
	s_waitcnt lgkmcnt(0)
	v_mfma_f32_32x32x16_bf16 v[96:111], v[210:213], v[140:143], v[96:111]
	ds_read_b128 v[128:131], v189 offset:0
	ds_read_b128 v[132:135], v189 offset:0x2000
	ds_read_b128 v[136:139], v181 offset:0
	ds_read_b128 v[198:201], v188 offset:0
	ds_read_b128 v[202:205], v188 offset:0x2000
	ds_read_b128 v[206:209], v181 offset:0x400
	s_waitcnt lgkmcnt(3)
	s_nop 0
	v_mfma_f32_32x32x16_bf16 v[144:159], v[128:131], v[136:139], 0
	v_mfma_f32_32x32x16_bf16 v[128:143], v[132:135], v[136:139], 0
	ds_read_b128 v[210:213], v187 offset:0
	ds_read_b128 v[214:217], v187 offset:0x2000
	ds_read_b128 v[218:221], v181 offset:0x800
	s_waitcnt lgkmcnt(3)
	v_mfma_f32_32x32x16_bf16 v[144:159], v[198:201], v[206:209], v[144:159]
	v_mfma_f32_32x32x16_bf16 v[128:143], v[202:205], v[206:209], v[128:143]
	ds_read_b128 v[198:201], v186 offset:0
	ds_read_b128 v[202:205], v186 offset:0x2000
	ds_read_b128 v[206:209], v181 offset:0xc00
	s_waitcnt lgkmcnt(3)
	v_mfma_f32_32x32x16_bf16 v[144:159], v[210:213], v[218:221], v[144:159]
	v_mfma_f32_32x32x16_bf16 v[128:143], v[214:217], v[218:221], v[128:143]
	ds_read_b128 v[210:213], v189 offset:0x80
	ds_read_b128 v[214:217], v189 offset:0x2080
	ds_read_b128 v[218:221], v181 offset:0x1000
	s_waitcnt lgkmcnt(3)
	v_mfma_f32_32x32x16_bf16 v[144:159], v[198:201], v[206:209], v[144:159]
	v_mfma_f32_32x32x16_bf16 v[128:143], v[202:205], v[206:209], v[128:143]
	ds_read_b128 v[198:201], v188 offset:0x80
	ds_read_b128 v[202:205], v188 offset:0x2080
	ds_read_b128 v[206:209], v181 offset:0x1400
	s_waitcnt lgkmcnt(3)
	v_mfma_f32_32x32x16_bf16 v[144:159], v[210:213], v[218:221], v[144:159]
	v_mfma_f32_32x32x16_bf16 v[128:143], v[214:217], v[218:221], v[128:143]
	ds_read_b128 v[210:213], v187 offset:0x80
	ds_read_b128 v[214:217], v187 offset:0x2080
	ds_read_b128 v[218:221], v181 offset:0x1800
	s_waitcnt lgkmcnt(3)
	v_mfma_f32_32x32x16_bf16 v[144:159], v[198:201], v[206:209], v[144:159]
	v_mfma_f32_32x32x16_bf16 v[128:143], v[202:205], v[206:209], v[128:143]
	ds_read_b128 v[198:201], v186 offset:0x80
	ds_read_b128 v[202:205], v186 offset:0x2080
	s_waitcnt lgkmcnt(2)
	v_mfma_f32_32x32x16_bf16 v[144:159], v[210:213], v[218:221], v[144:159]
	v_mfma_f32_32x32x16_bf16 v[128:143], v[214:217], v[218:221], v[128:143]
	s_waitcnt lgkmcnt(0)
	v_mfma_f32_32x32x16_bf16 v[144:159], v[198:201], v[166:169], v[144:159]
	v_mfma_f32_32x32x16_bf16 v[128:143], v[202:205], v[166:169], v[128:143]
	s_bitcmp0_b32 s100, 8
	s_cbranch_scc1 .Lstg_a2
	s_waitcnt vmcnt(0)
	s_waitcnt lgkmcnt(0)
	s_barrier

.LBB0_526:
	s_add_u32 s33, s72, s84
	s_addc_u32 s92, s73, s90
	s_add_u32 s4, s33, 0x2dd40800
	s_addc_u32 s5, s92, 0
	s_mov_b32 m0, s81
	s_nop 0
	global_load_lds_dwordx4 v162, s[4:5]
	s_add_i32 m0, s78, 0xffffff80
	s_nop 0
	global_load_lds_dwordx4 v162, s[4:5] offset:128
	s_add_i32 m0, s69, 0xffffff00
	s_nop 0
	global_load_lds_dwordx4 v162, s[4:5] offset:256
	s_add_i32 m0, s68, 0xfffffe80
	s_nop 0
	global_load_lds_dwordx4 v162, s[4:5] offset:384
	ds_read_b64_tr_b16 v[144:145], v177 offset:0x8000
	ds_read_b64_tr_b16 v[146:147], v177 offset:0x9000
	ds_read_b64_tr_b16 v[148:149], v177 offset:0xa000
	ds_read_b64_tr_b16 v[150:151], v177 offset:0xb000
	ds_read_b64_tr_b16 v[152:153], v177 offset:0xc000
	ds_read_b64_tr_b16 v[154:155], v177 offset:0xd000
	ds_read_b64_tr_b16 v[156:157], v177 offset:0xe000
	ds_read_b64_tr_b16 v[158:159], v177 offset:0xf000
	s_waitcnt lgkmcnt(6)
	s_nop 1
	v_mfma_f32_32x32x16_bf16 v[112:127], v[144:147], v[128:131], v[112:127]
	ds_read_b64_tr_b16 v[236:237], v177 offset:0x8200
	ds_read_b64_tr_b16 v[238:239], v177 offset:0x9200
	s_waitcnt lgkmcnt(6)
	v_mfma_f32_32x32x16_bf16 v[112:127], v[148:151], v[132:135], v[112:127]
	ds_read_b64_tr_b16 v[240:241], v177 offset:0xa200
	ds_read_b64_tr_b16 v[242:243], v177 offset:0xb200
	s_waitcnt lgkmcnt(6)
	v_mfma_f32_32x32x16_bf16 v[112:127], v[152:155], v[136:139], v[112:127]
	ds_read_b64_tr_b16 v[244:245], v177 offset:0xc200
	ds_read_b64_tr_b16 v[246:247], v177 offset:0xd200
	s_waitcnt lgkmcnt(6)
	v_mfma_f32_32x32x16_bf16 v[112:127], v[156:159], v[140:143], v[112:127]
	ds_read_b64_tr_b16 v[248:249], v177 offset:0xe200
	ds_read_b64_tr_b16 v[250:251], v177 offset:0xf200
	s_waitcnt lgkmcnt(6)
	v_mfma_f32_32x32x16_bf16 v[0:15], v[236:239], v[128:131], v[0:15]
	ds_read_b64_tr_b16 v[144:145], v177 offset:0x8400
	ds_read_b64_tr_b16 v[146:147], v177 offset:0x9400
	s_waitcnt lgkmcnt(6)
	v_mfma_f32_32x32x16_bf16 v[0:15], v[240:243], v[132:135], v[0:15]
	ds_read_b64_tr_b16 v[148:149], v177 offset:0xa400
	ds_read_b64_tr_b16 v[150:151], v177 offset:0xb400
	s_waitcnt lgkmcnt(6)
	v_mfma_f32_32x32x16_bf16 v[0:15], v[244:247], v[136:139], v[0:15]
	ds_read_b64_tr_b16 v[152:153], v177 offset:0xc400
	ds_read_b64_tr_b16 v[154:155], v177 offset:0xd400
	s_waitcnt lgkmcnt(6)
	v_mfma_f32_32x32x16_bf16 v[0:15], v[248:251], v[140:143], v[0:15]
	ds_read_b64_tr_b16 v[156:157], v177 offset:0xe400
	ds_read_b64_tr_b16 v[158:159], v177 offset:0xf400
	s_waitcnt lgkmcnt(6)
	v_mfma_f32_32x32x16_bf16 v[16:31], v[144:147], v[128:131], v[16:31]
	ds_read_b64_tr_b16 v[236:237], v177 offset:0x8600
	ds_read_b64_tr_b16 v[238:239], v177 offset:0x9600
	s_waitcnt lgkmcnt(6)
	v_mfma_f32_32x32x16_bf16 v[16:31], v[148:151], v[132:135], v[16:31]
	ds_read_b64_tr_b16 v[240:241], v177 offset:0xa600
	ds_read_b64_tr_b16 v[242:243], v177 offset:0xb600
	s_waitcnt lgkmcnt(6)
	v_mfma_f32_32x32x16_bf16 v[16:31], v[152:155], v[136:139], v[16:31]
	ds_read_b64_tr_b16 v[244:245], v177 offset:0xc600
	ds_read_b64_tr_b16 v[246:247], v177 offset:0xd600
	s_waitcnt lgkmcnt(6)
	v_mfma_f32_32x32x16_bf16 v[16:31], v[156:159], v[140:143], v[16:31]
	ds_read_b64_tr_b16 v[248:249], v177 offset:0xe600
	ds_read_b64_tr_b16 v[250:251], v177 offset:0xf600
	s_waitcnt lgkmcnt(6)
	v_mfma_f32_32x32x16_bf16 v[32:47], v[236:239], v[128:131], v[32:47]
	ds_read_b64_tr_b16 v[144:145], v177 offset:0x8800
	ds_read_b64_tr_b16 v[146:147], v177 offset:0x9800
	s_waitcnt lgkmcnt(6)
	v_mfma_f32_32x32x16_bf16 v[32:47], v[240:243], v[132:135], v[32:47]
	ds_read_b64_tr_b16 v[148:149], v177 offset:0xa800
	ds_read_b64_tr_b16 v[150:151], v177 offset:0xb800
	s_waitcnt lgkmcnt(6)
	v_mfma_f32_32x32x16_bf16 v[32:47], v[244:247], v[136:139], v[32:47]
	ds_read_b64_tr_b16 v[152:153], v177 offset:0xc800
	ds_read_b64_tr_b16 v[154:155], v177 offset:0xd800
	s_waitcnt lgkmcnt(6)
	v_mfma_f32_32x32x16_bf16 v[32:47], v[248:251], v[140:143], v[32:47]
	ds_read_b64_tr_b16 v[156:157], v177 offset:0xe800
	ds_read_b64_tr_b16 v[158:159], v177 offset:0xf800
	s_waitcnt lgkmcnt(6)
	v_mfma_f32_32x32x16_bf16 v[48:63], v[144:147], v[128:131], v[48:63]
	ds_read_b64_tr_b16 v[236:237], v177 offset:0x8a00
	ds_read_b64_tr_b16 v[238:239], v177 offset:0x9a00
	s_waitcnt lgkmcnt(6)
	v_mfma_f32_32x32x16_bf16 v[48:63], v[148:151], v[132:135], v[48:63]
	ds_read_b64_tr_b16 v[240:241], v177 offset:0xaa00
	ds_read_b64_tr_b16 v[242:243], v177 offset:0xba00
	s_waitcnt lgkmcnt(6)
	v_mfma_f32_32x32x16_bf16 v[48:63], v[152:155], v[136:139], v[48:63]
	ds_read_b64_tr_b16 v[244:245], v177 offset:0xca00
	ds_read_b64_tr_b16 v[246:247], v177 offset:0xda00
	s_waitcnt lgkmcnt(6)
	v_mfma_f32_32x32x16_bf16 v[48:63], v[156:159], v[140:143], v[48:63]
	ds_read_b64_tr_b16 v[248:249], v177 offset:0xea00
	ds_read_b64_tr_b16 v[250:251], v177 offset:0xfa00
	s_waitcnt lgkmcnt(6)
	v_mfma_f32_32x32x16_bf16 v[64:79], v[236:239], v[128:131], v[64:79]
	ds_read_b64_tr_b16 v[144:145], v177 offset:0x8c00
	ds_read_b64_tr_b16 v[146:147], v177 offset:0x9c00
	s_waitcnt lgkmcnt(6)
	v_mfma_f32_32x32x16_bf16 v[64:79], v[240:243], v[132:135], v[64:79]
	ds_read_b64_tr_b16 v[148:149], v177 offset:0xac00
	ds_read_b64_tr_b16 v[150:151], v177 offset:0xbc00
	s_waitcnt lgkmcnt(6)
	v_mfma_f32_32x32x16_bf16 v[64:79], v[244:247], v[136:139], v[64:79]
	ds_read_b64_tr_b16 v[152:153], v177 offset:0xcc00
	ds_read_b64_tr_b16 v[154:155], v177 offset:0xdc00
	s_waitcnt lgkmcnt(6)
	v_mfma_f32_32x32x16_bf16 v[64:79], v[248:251], v[140:143], v[64:79]
	ds_read_b64_tr_b16 v[156:157], v177 offset:0xec00
	ds_read_b64_tr_b16 v[158:159], v177 offset:0xfc00
	s_waitcnt lgkmcnt(6)
	v_mfma_f32_32x32x16_bf16 v[80:95], v[144:147], v[128:131], v[80:95]
	ds_read_b64_tr_b16 v[236:237], v177 offset:0x8e00
	ds_read_b64_tr_b16 v[238:239], v177 offset:0x9e00
	s_waitcnt lgkmcnt(6)
	v_mfma_f32_32x32x16_bf16 v[80:95], v[148:151], v[132:135], v[80:95]
	ds_read_b64_tr_b16 v[240:241], v177 offset:0xae00
	ds_read_b64_tr_b16 v[242:243], v177 offset:0xbe00
	s_waitcnt lgkmcnt(6)
	v_mfma_f32_32x32x16_bf16 v[80:95], v[152:155], v[136:139], v[80:95]
	ds_read_b64_tr_b16 v[244:245], v177 offset:0xce00
	ds_read_b64_tr_b16 v[246:247], v177 offset:0xde00
	s_waitcnt lgkmcnt(6)
	v_mfma_f32_32x32x16_bf16 v[80:95], v[156:159], v[140:143], v[80:95]
	ds_read_b64_tr_b16 v[248:249], v177 offset:0xee00
	ds_read_b64_tr_b16 v[250:251], v177 offset:0xfe00
	s_waitcnt lgkmcnt(6)
	v_mfma_f32_32x32x16_bf16 v[96:111], v[236:239], v[128:131], v[96:111]
	s_waitcnt lgkmcnt(4)
	v_mfma_f32_32x32x16_bf16 v[96:111], v[240:243], v[132:135], v[96:111]
	s_waitcnt lgkmcnt(2)
	v_mfma_f32_32x32x16_bf16 v[96:111], v[244:247], v[136:139], v[96:111]
	s_waitcnt lgkmcnt(0)
	v_mfma_f32_32x32x16_bf16 v[96:111], v[248:251], v[140:143], v[96:111]
	ds_read_b128 v[128:131], v182 offset:0
	ds_read_b128 v[132:135], v182 offset:0x2000
	ds_read_b128 v[136:139], v181 offset:0
	ds_read_b128 v[236:239], v183 offset:0
	ds_read_b128 v[240:243], v183 offset:0x2000
	ds_read_b128 v[244:247], v181 offset:0x400
	s_waitcnt lgkmcnt(3)
	s_nop 0
	v_mfma_f32_32x32x16_bf16 v[144:159], v[128:131], v[136:139], 0
	v_mfma_f32_32x32x16_bf16 v[128:143], v[132:135], v[136:139], 0
	ds_read_b128 v[248:251], v184 offset:0
	ds_read_b128 v[194:197], v184 offset:0x2000
	ds_read_b128 v[222:225], v181 offset:0x800
	s_waitcnt lgkmcnt(3)
	v_mfma_f32_32x32x16_bf16 v[144:159], v[236:239], v[244:247], v[144:159]
	v_mfma_f32_32x32x16_bf16 v[128:143], v[240:243], v[244:247], v[128:143]
	ds_read_b128 v[236:239], v185 offset:0
	ds_read_b128 v[240:243], v185 offset:0x2000
	ds_read_b128 v[244:247], v181 offset:0xc00
	s_waitcnt lgkmcnt(3)
	v_mfma_f32_32x32x16_bf16 v[144:159], v[248:251], v[222:225], v[144:159]
	v_mfma_f32_32x32x16_bf16 v[128:143], v[194:197], v[222:225], v[128:143]
	ds_read_b128 v[194:197], v182 offset:0x80
	ds_read_b128 v[222:225], v182 offset:0x2080
	ds_read_b128 v[248:251], v181 offset:0x1000
	s_waitcnt lgkmcnt(3)
	v_mfma_f32_32x32x16_bf16 v[144:159], v[236:239], v[244:247], v[144:159]
	v_mfma_f32_32x32x16_bf16 v[128:143], v[240:243], v[244:247], v[128:143]
	ds_read_b128 v[236:239], v183 offset:0x80
	ds_read_b128 v[240:243], v183 offset:0x2080
	ds_read_b128 v[244:247], v181 offset:0x1400
	s_waitcnt lgkmcnt(3)
	v_mfma_f32_32x32x16_bf16 v[144:159], v[194:197], v[248:251], v[144:159]
	v_mfma_f32_32x32x16_bf16 v[128:143], v[222:225], v[248:251], v[128:143]
	ds_read_b128 v[194:197], v184 offset:0x80
	ds_read_b128 v[222:225], v184 offset:0x2080
	ds_read_b128 v[248:251], v181 offset:0x1800
	s_waitcnt lgkmcnt(3)
	v_mfma_f32_32x32x16_bf16 v[144:159], v[236:239], v[244:247], v[144:159]
	v_mfma_f32_32x32x16_bf16 v[128:143], v[240:243], v[244:247], v[128:143]
	ds_read_b128 v[236:239], v185 offset:0x80
	ds_read_b128 v[240:243], v185 offset:0x2080
	s_waitcnt lgkmcnt(2)
	v_mfma_f32_32x32x16_bf16 v[144:159], v[194:197], v[248:251], v[144:159]
	v_mfma_f32_32x32x16_bf16 v[128:143], v[222:225], v[248:251], v[128:143]
	s_waitcnt lgkmcnt(0)
	v_mfma_f32_32x32x16_bf16 v[144:159], v[236:239], v[166:169], v[144:159]
	v_mfma_f32_32x32x16_bf16 v[128:143], v[240:243], v[166:169], v[128:143]
	s_bitcmp0_b32 s100, 8
	s_cbranch_scc1 .Lstg_a3
	s_waitcnt vmcnt(0)
	s_waitcnt lgkmcnt(0)
	s_barrier

.LBB0_539:
	ds_read_b64_tr_b16 v[144:145], v177 offset:0
	ds_read_b64_tr_b16 v[146:147], v177 offset:0x1000
	ds_read_b64_tr_b16 v[148:149], v177 offset:0x2000
	ds_read_b64_tr_b16 v[150:151], v177 offset:0x3000
	ds_read_b64_tr_b16 v[152:153], v177 offset:0x4000
	ds_read_b64_tr_b16 v[154:155], v177 offset:0x5000
	ds_read_b64_tr_b16 v[156:157], v177 offset:0x6000
	ds_read_b64_tr_b16 v[158:159], v177 offset:0x7000
	s_waitcnt lgkmcnt(6)
	s_nop 0
	v_mfma_f32_32x32x16_bf16 v[112:127], v[144:147], v[128:131], v[112:127]
	ds_read_b64_tr_b16 v[170:171], v177 offset:0x200
	ds_read_b64_tr_b16 v[172:173], v177 offset:0x1200
	s_waitcnt lgkmcnt(6)
	v_mfma_f32_32x32x16_bf16 v[112:127], v[148:151], v[132:135], v[112:127]
	ds_read_b64_tr_b16 v[182:183], v177 offset:0x2200
	ds_read_b64_tr_b16 v[184:185], v177 offset:0x3200
	s_waitcnt lgkmcnt(6)
	v_mfma_f32_32x32x16_bf16 v[112:127], v[152:155], v[136:139], v[112:127]
	ds_read_b64_tr_b16 v[190:191], v177 offset:0x4200
	ds_read_b64_tr_b16 v[192:193], v177 offset:0x5200
	s_waitcnt lgkmcnt(6)
	v_mfma_f32_32x32x16_bf16 v[112:127], v[156:159], v[140:143], v[112:127]
	ds_read_b64_tr_b16 v[198:199], v177 offset:0x6200
	ds_read_b64_tr_b16 v[200:201], v177 offset:0x7200
	s_waitcnt lgkmcnt(6)
	v_mfma_f32_32x32x16_bf16 v[0:15], v[170:173], v[128:131], v[0:15]
	ds_read_b64_tr_b16 v[144:145], v177 offset:0x400
	ds_read_b64_tr_b16 v[146:147], v177 offset:0x1400
	s_waitcnt lgkmcnt(6)
	v_mfma_f32_32x32x16_bf16 v[0:15], v[182:185], v[132:135], v[0:15]
	ds_read_b64_tr_b16 v[148:149], v177 offset:0x2400
	ds_read_b64_tr_b16 v[150:151], v177 offset:0x3400
	s_waitcnt lgkmcnt(6)
	v_mfma_f32_32x32x16_bf16 v[0:15], v[190:193], v[136:139], v[0:15]
	ds_read_b64_tr_b16 v[152:153], v177 offset:0x4400
	ds_read_b64_tr_b16 v[154:155], v177 offset:0x5400
	s_waitcnt lgkmcnt(6)
	v_mfma_f32_32x32x16_bf16 v[0:15], v[198:201], v[140:143], v[0:15]
	ds_read_b64_tr_b16 v[156:157], v177 offset:0x6400
	ds_read_b64_tr_b16 v[158:159], v177 offset:0x7400
	s_waitcnt lgkmcnt(6)
	v_mfma_f32_32x32x16_bf16 v[16:31], v[144:147], v[128:131], v[16:31]
	ds_read_b64_tr_b16 v[170:171], v177 offset:0x600
	ds_read_b64_tr_b16 v[172:173], v177 offset:0x1600
	s_waitcnt lgkmcnt(6)
	v_mfma_f32_32x32x16_bf16 v[16:31], v[148:151], v[132:135], v[16:31]
	ds_read_b64_tr_b16 v[182:183], v177 offset:0x2600
	ds_read_b64_tr_b16 v[184:185], v177 offset:0x3600
	s_waitcnt lgkmcnt(6)
	v_mfma_f32_32x32x16_bf16 v[16:31], v[152:155], v[136:139], v[16:31]
	ds_read_b64_tr_b16 v[190:191], v177 offset:0x4600
	ds_read_b64_tr_b16 v[192:193], v177 offset:0x5600
	s_waitcnt lgkmcnt(6)
	v_mfma_f32_32x32x16_bf16 v[16:31], v[156:159], v[140:143], v[16:31]
	ds_read_b64_tr_b16 v[198:199], v177 offset:0x6600
	ds_read_b64_tr_b16 v[200:201], v177 offset:0x7600
	s_waitcnt lgkmcnt(6)
	v_mfma_f32_32x32x16_bf16 v[32:47], v[170:173], v[128:131], v[32:47]
	ds_read_b64_tr_b16 v[144:145], v177 offset:0x800
	ds_read_b64_tr_b16 v[146:147], v177 offset:0x1800
	s_waitcnt lgkmcnt(6)
	v_mfma_f32_32x32x16_bf16 v[32:47], v[182:185], v[132:135], v[32:47]
	ds_read_b64_tr_b16 v[148:149], v177 offset:0x2800
	ds_read_b64_tr_b16 v[150:151], v177 offset:0x3800
	s_waitcnt lgkmcnt(6)
	v_mfma_f32_32x32x16_bf16 v[32:47], v[190:193], v[136:139], v[32:47]
	ds_read_b64_tr_b16 v[152:153], v177 offset:0x4800
	ds_read_b64_tr_b16 v[154:155], v177 offset:0x5800
	s_waitcnt lgkmcnt(6)
	v_mfma_f32_32x32x16_bf16 v[32:47], v[198:201], v[140:143], v[32:47]
	ds_read_b64_tr_b16 v[156:157], v177 offset:0x6800
	ds_read_b64_tr_b16 v[158:159], v177 offset:0x7800
	s_waitcnt lgkmcnt(6)
	v_mfma_f32_32x32x16_bf16 v[48:63], v[144:147], v[128:131], v[48:63]
	ds_read_b64_tr_b16 v[170:171], v177 offset:0xa00
	ds_read_b64_tr_b16 v[172:173], v177 offset:0x1a00
	s_waitcnt lgkmcnt(6)
	v_mfma_f32_32x32x16_bf16 v[48:63], v[148:151], v[132:135], v[48:63]
	ds_read_b64_tr_b16 v[182:183], v177 offset:0x2a00
	ds_read_b64_tr_b16 v[184:185], v177 offset:0x3a00
	s_waitcnt lgkmcnt(6)
	v_mfma_f32_32x32x16_bf16 v[48:63], v[152:155], v[136:139], v[48:63]
	ds_read_b64_tr_b16 v[190:191], v177 offset:0x4a00
	ds_read_b64_tr_b16 v[192:193], v177 offset:0x5a00
	s_waitcnt lgkmcnt(6)
	v_mfma_f32_32x32x16_bf16 v[48:63], v[156:159], v[140:143], v[48:63]
	ds_read_b64_tr_b16 v[198:199], v177 offset:0x6a00
	ds_read_b64_tr_b16 v[200:201], v177 offset:0x7a00
	s_waitcnt lgkmcnt(6)
	v_mfma_f32_32x32x16_bf16 v[64:79], v[170:173], v[128:131], v[64:79]
	ds_read_b64_tr_b16 v[144:145], v177 offset:0xc00
	ds_read_b64_tr_b16 v[146:147], v177 offset:0x1c00
	s_waitcnt lgkmcnt(6)
	v_mfma_f32_32x32x16_bf16 v[64:79], v[182:185], v[132:135], v[64:79]
	ds_read_b64_tr_b16 v[148:149], v177 offset:0x2c00
	ds_read_b64_tr_b16 v[150:151], v177 offset:0x3c00
	s_waitcnt lgkmcnt(6)
	v_mfma_f32_32x32x16_bf16 v[64:79], v[190:193], v[136:139], v[64:79]
	ds_read_b64_tr_b16 v[152:153], v177 offset:0x4c00
	ds_read_b64_tr_b16 v[154:155], v177 offset:0x5c00
	s_waitcnt lgkmcnt(6)
	v_mfma_f32_32x32x16_bf16 v[64:79], v[198:201], v[140:143], v[64:79]
	ds_read_b64_tr_b16 v[156:157], v177 offset:0x6c00
	ds_read_b64_tr_b16 v[158:159], v177 offset:0x7c00
	s_waitcnt lgkmcnt(6)
	v_mfma_f32_32x32x16_bf16 v[80:95], v[144:147], v[128:131], v[80:95]
	ds_read_b64_tr_b16 v[170:171], v177 offset:0xe00
	ds_read_b64_tr_b16 v[172:173], v177 offset:0x1e00
	s_waitcnt lgkmcnt(6)
	v_mfma_f32_32x32x16_bf16 v[80:95], v[148:151], v[132:135], v[80:95]
	ds_read_b64_tr_b16 v[182:183], v177 offset:0x2e00
	ds_read_b64_tr_b16 v[184:185], v177 offset:0x3e00
	s_waitcnt lgkmcnt(6)
	v_mfma_f32_32x32x16_bf16 v[80:95], v[152:155], v[136:139], v[80:95]
	ds_read_b64_tr_b16 v[190:191], v177 offset:0x4e00
	ds_read_b64_tr_b16 v[192:193], v177 offset:0x5e00
	s_waitcnt lgkmcnt(6)
	v_mfma_f32_32x32x16_bf16 v[80:95], v[156:159], v[140:143], v[80:95]
	ds_read_b64_tr_b16 v[198:199], v177 offset:0x6e00
	ds_read_b64_tr_b16 v[200:201], v177 offset:0x7e00
	s_waitcnt lgkmcnt(6)
	v_mfma_f32_32x32x16_bf16 v[96:111], v[170:173], v[128:131], v[96:111]
	s_waitcnt lgkmcnt(4)
	v_mfma_f32_32x32x16_bf16 v[96:111], v[182:185], v[132:135], v[96:111]
	s_waitcnt lgkmcnt(2)
	v_mfma_f32_32x32x16_bf16 v[96:111], v[190:193], v[136:139], v[96:111]
	s_waitcnt lgkmcnt(0)
	v_mfma_f32_32x32x16_bf16 v[96:111], v[198:201], v[140:143], v[96:111]
	ds_read_b128 v[128:131], v189 offset:0
	ds_read_b128 v[132:135], v189 offset:0x2000
	ds_read_b128 v[136:139], v181 offset:0
	ds_read_b128 v[170:173], v188 offset:0
	ds_read_b128 v[182:185], v188 offset:0x2000
	ds_read_b128 v[190:193], v181 offset:0x400
	s_waitcnt lgkmcnt(3)
	s_nop 0
	v_mfma_f32_32x32x16_bf16 v[144:159], v[128:131], v[136:139], 0
	v_mfma_f32_32x32x16_bf16 v[128:143], v[132:135], v[136:139], 0
	ds_read_b128 v[198:201], v187 offset:0
	ds_read_b128 v[202:205], v187 offset:0x2000
	ds_read_b128 v[206:209], v181 offset:0x800
	s_waitcnt lgkmcnt(3)
	v_mfma_f32_32x32x16_bf16 v[144:159], v[170:173], v[190:193], v[144:159]
	v_mfma_f32_32x32x16_bf16 v[128:143], v[182:185], v[190:193], v[128:143]
	ds_read_b128 v[170:173], v186 offset:0
	ds_read_b128 v[182:185], v186 offset:0x2000
	ds_read_b128 v[190:193], v181 offset:0xc00
	s_waitcnt lgkmcnt(3)
	v_mfma_f32_32x32x16_bf16 v[144:159], v[198:201], v[206:209], v[144:159]
	v_mfma_f32_32x32x16_bf16 v[128:143], v[202:205], v[206:209], v[128:143]
	ds_read_b128 v[198:201], v189 offset:0x80
	ds_read_b128 v[202:205], v189 offset:0x2080
	ds_read_b128 v[206:209], v181 offset:0x1000
	s_waitcnt lgkmcnt(3)
	v_mfma_f32_32x32x16_bf16 v[144:159], v[170:173], v[190:193], v[144:159]
	v_mfma_f32_32x32x16_bf16 v[128:143], v[182:185], v[190:193], v[128:143]
	ds_read_b128 v[170:173], v188 offset:0x80
	ds_read_b128 v[182:185], v188 offset:0x2080
	ds_read_b128 v[188:191], v181 offset:0x1400
	s_waitcnt lgkmcnt(3)
	v_mfma_f32_32x32x16_bf16 v[144:159], v[198:201], v[206:209], v[144:159]
	v_mfma_f32_32x32x16_bf16 v[128:143], v[202:205], v[206:209], v[128:143]
	ds_read_b128 v[198:201], v187 offset:0x80
	ds_read_b128 v[202:205], v187 offset:0x2080
	ds_read_b128 v[206:209], v181 offset:0x1800
	s_waitcnt lgkmcnt(3)
	v_mfma_f32_32x32x16_bf16 v[144:159], v[170:173], v[188:191], v[144:159]
	v_mfma_f32_32x32x16_bf16 v[128:143], v[182:185], v[188:191], v[128:143]
	ds_read_b128 v[170:173], v186 offset:0x80
	ds_read_b128 v[182:185], v186 offset:0x2080
	s_waitcnt lgkmcnt(2)
	v_mfma_f32_32x32x16_bf16 v[144:159], v[198:201], v[206:209], v[144:159]
	v_mfma_f32_32x32x16_bf16 v[128:143], v[202:205], v[206:209], v[128:143]
	s_waitcnt lgkmcnt(0)
	v_mfma_f32_32x32x16_bf16 v[144:159], v[170:173], v[166:169], v[144:159]
	v_mfma_f32_32x32x16_bf16 v[128:143], v[182:185], v[166:169], v[128:143]
	s_bitcmp0_b32 s100, 8
	s_cbranch_scc1 .Lstg_a4
	s_waitcnt vmcnt(0)
	s_waitcnt lgkmcnt(0)
	s_barrier

.LBB0_557:
	ds_read_b64_tr_b16 v[144:145], v177 offset:0
	ds_read_b64_tr_b16 v[146:147], v177 offset:0x1000
	ds_read_b64_tr_b16 v[148:149], v177 offset:0x2000
	ds_read_b64_tr_b16 v[150:151], v177 offset:0x3000
	ds_read_b64_tr_b16 v[152:153], v177 offset:0x4000
	ds_read_b64_tr_b16 v[154:155], v177 offset:0x5000
	ds_read_b64_tr_b16 v[156:157], v177 offset:0x6000
	ds_read_b64_tr_b16 v[158:159], v177 offset:0x7000
	s_waitcnt lgkmcnt(6)
	s_nop 0
	v_mfma_f32_32x32x16_bf16 v[112:127], v[144:147], v[128:131], v[112:127]
	ds_read_b64_tr_b16 v[192:193], v177 offset:0x200
	ds_read_b64_tr_b16 v[194:195], v177 offset:0x1200
	s_waitcnt lgkmcnt(6)
	v_mfma_f32_32x32x16_bf16 v[112:127], v[148:151], v[132:135], v[112:127]
	ds_read_b64_tr_b16 v[196:197], v177 offset:0x2200
	ds_read_b64_tr_b16 v[198:199], v177 offset:0x3200
	s_waitcnt lgkmcnt(6)
	v_mfma_f32_32x32x16_bf16 v[112:127], v[152:155], v[136:139], v[112:127]
	ds_read_b64_tr_b16 v[200:201], v177 offset:0x4200
	ds_read_b64_tr_b16 v[202:203], v177 offset:0x5200
	s_waitcnt lgkmcnt(6)
	v_mfma_f32_32x32x16_bf16 v[112:127], v[156:159], v[140:143], v[112:127]
	ds_read_b64_tr_b16 v[204:205], v177 offset:0x6200
	ds_read_b64_tr_b16 v[206:207], v177 offset:0x7200
	s_waitcnt lgkmcnt(6)
	v_mfma_f32_32x32x16_bf16 v[80:95], v[192:195], v[128:131], v[80:95]
	ds_read_b64_tr_b16 v[144:145], v177 offset:0x400
	ds_read_b64_tr_b16 v[146:147], v177 offset:0x1400
	s_waitcnt lgkmcnt(6)
	v_mfma_f32_32x32x16_bf16 v[80:95], v[196:199], v[132:135], v[80:95]
	ds_read_b64_tr_b16 v[148:149], v177 offset:0x2400
	ds_read_b64_tr_b16 v[150:151], v177 offset:0x3400
	s_waitcnt lgkmcnt(6)
	v_mfma_f32_32x32x16_bf16 v[80:95], v[200:203], v[136:139], v[80:95]
	ds_read_b64_tr_b16 v[152:153], v177 offset:0x4400
	ds_read_b64_tr_b16 v[154:155], v177 offset:0x5400
	s_waitcnt lgkmcnt(6)
	v_mfma_f32_32x32x16_bf16 v[80:95], v[204:207], v[140:143], v[80:95]
	ds_read_b64_tr_b16 v[156:157], v177 offset:0x6400
	ds_read_b64_tr_b16 v[158:159], v177 offset:0x7400
	s_waitcnt lgkmcnt(6)
	v_mfma_f32_32x32x16_bf16 v[96:111], v[144:147], v[128:131], v[96:111]
	ds_read_b64_tr_b16 v[192:193], v177 offset:0x600
	ds_read_b64_tr_b16 v[194:195], v177 offset:0x1600
	s_waitcnt lgkmcnt(6)
	v_mfma_f32_32x32x16_bf16 v[96:111], v[148:151], v[132:135], v[96:111]
	ds_read_b64_tr_b16 v[196:197], v177 offset:0x2600
	ds_read_b64_tr_b16 v[198:199], v177 offset:0x3600
	s_waitcnt lgkmcnt(6)
	v_mfma_f32_32x32x16_bf16 v[96:111], v[152:155], v[136:139], v[96:111]
	ds_read_b64_tr_b16 v[200:201], v177 offset:0x4600
	ds_read_b64_tr_b16 v[202:203], v177 offset:0x5600
	s_waitcnt lgkmcnt(6)
	v_mfma_f32_32x32x16_bf16 v[96:111], v[156:159], v[140:143], v[96:111]
	ds_read_b64_tr_b16 v[204:205], v177 offset:0x6600
	ds_read_b64_tr_b16 v[206:207], v177 offset:0x7600
	s_waitcnt lgkmcnt(6)
	v_mfma_f32_32x32x16_bf16 v[64:79], v[192:195], v[128:131], v[64:79]
	ds_read_b64_tr_b16 v[144:145], v177 offset:0x800
	ds_read_b64_tr_b16 v[146:147], v177 offset:0x1800
	s_waitcnt lgkmcnt(6)
	v_mfma_f32_32x32x16_bf16 v[64:79], v[196:199], v[132:135], v[64:79]
	ds_read_b64_tr_b16 v[148:149], v177 offset:0x2800
	ds_read_b64_tr_b16 v[150:151], v177 offset:0x3800
	s_waitcnt lgkmcnt(6)
	v_mfma_f32_32x32x16_bf16 v[64:79], v[200:203], v[136:139], v[64:79]
	ds_read_b64_tr_b16 v[152:153], v177 offset:0x4800
	ds_read_b64_tr_b16 v[154:155], v177 offset:0x5800
	s_waitcnt lgkmcnt(6)
	v_mfma_f32_32x32x16_bf16 v[64:79], v[204:207], v[140:143], v[64:79]
	ds_read_b64_tr_b16 v[156:157], v177 offset:0x6800
	ds_read_b64_tr_b16 v[158:159], v177 offset:0x7800
	s_waitcnt lgkmcnt(6)
	v_mfma_f32_32x32x16_bf16 v[48:63], v[144:147], v[128:131], v[48:63]
	ds_read_b64_tr_b16 v[192:193], v177 offset:0xa00
	ds_read_b64_tr_b16 v[194:195], v177 offset:0x1a00
	s_waitcnt lgkmcnt(6)
	v_mfma_f32_32x32x16_bf16 v[48:63], v[148:151], v[132:135], v[48:63]
	ds_read_b64_tr_b16 v[196:197], v177 offset:0x2a00
	ds_read_b64_tr_b16 v[198:199], v177 offset:0x3a00
	s_waitcnt lgkmcnt(6)
	v_mfma_f32_32x32x16_bf16 v[48:63], v[152:155], v[136:139], v[48:63]
	ds_read_b64_tr_b16 v[200:201], v177 offset:0x4a00
	ds_read_b64_tr_b16 v[202:203], v177 offset:0x5a00
	s_waitcnt lgkmcnt(6)
	v_mfma_f32_32x32x16_bf16 v[48:63], v[156:159], v[140:143], v[48:63]
	ds_read_b64_tr_b16 v[204:205], v177 offset:0x6a00
	ds_read_b64_tr_b16 v[206:207], v177 offset:0x7a00
	s_waitcnt lgkmcnt(6)
	v_mfma_f32_32x32x16_bf16 v[32:47], v[192:195], v[128:131], v[32:47]
	ds_read_b64_tr_b16 v[144:145], v177 offset:0xc00
	ds_read_b64_tr_b16 v[146:147], v177 offset:0x1c00
	s_waitcnt lgkmcnt(6)
	v_mfma_f32_32x32x16_bf16 v[32:47], v[196:199], v[132:135], v[32:47]
	ds_read_b64_tr_b16 v[148:149], v177 offset:0x2c00
	ds_read_b64_tr_b16 v[150:151], v177 offset:0x3c00
	s_waitcnt lgkmcnt(6)
	v_mfma_f32_32x32x16_bf16 v[32:47], v[200:203], v[136:139], v[32:47]
	ds_read_b64_tr_b16 v[152:153], v177 offset:0x4c00
	ds_read_b64_tr_b16 v[154:155], v177 offset:0x5c00
	s_waitcnt lgkmcnt(6)
	v_mfma_f32_32x32x16_bf16 v[32:47], v[204:207], v[140:143], v[32:47]
	ds_read_b64_tr_b16 v[156:157], v177 offset:0x6c00
	ds_read_b64_tr_b16 v[158:159], v177 offset:0x7c00
	s_waitcnt lgkmcnt(6)
	v_mfma_f32_32x32x16_bf16 v[16:31], v[144:147], v[128:131], v[16:31]
	ds_read_b64_tr_b16 v[192:193], v177 offset:0xe00
	ds_read_b64_tr_b16 v[194:195], v177 offset:0x1e00
	s_waitcnt lgkmcnt(6)
	v_mfma_f32_32x32x16_bf16 v[16:31], v[148:151], v[132:135], v[16:31]
	ds_read_b64_tr_b16 v[196:197], v177 offset:0x2e00
	ds_read_b64_tr_b16 v[198:199], v177 offset:0x3e00
	s_waitcnt lgkmcnt(6)
	v_mfma_f32_32x32x16_bf16 v[16:31], v[152:155], v[136:139], v[16:31]
	ds_read_b64_tr_b16 v[200:201], v177 offset:0x4e00
	ds_read_b64_tr_b16 v[202:203], v177 offset:0x5e00
	s_waitcnt lgkmcnt(6)
	v_mfma_f32_32x32x16_bf16 v[16:31], v[156:159], v[140:143], v[16:31]
	ds_read_b64_tr_b16 v[204:205], v177 offset:0x6e00
	ds_read_b64_tr_b16 v[206:207], v177 offset:0x7e00
	s_waitcnt lgkmcnt(6)
	v_mfma_f32_32x32x16_bf16 v[0:15], v[192:195], v[128:131], v[0:15]
	s_waitcnt lgkmcnt(4)
	v_mfma_f32_32x32x16_bf16 v[0:15], v[196:199], v[132:135], v[0:15]
	s_waitcnt lgkmcnt(2)
	v_mfma_f32_32x32x16_bf16 v[0:15], v[200:203], v[136:139], v[0:15]
	s_waitcnt lgkmcnt(0)
	v_mfma_f32_32x32x16_bf16 v[0:15], v[204:207], v[140:143], v[0:15]
	ds_read_b128 v[128:131], v188 offset:0
	ds_read_b128 v[132:135], v188 offset:0x2000
	ds_read_b128 v[136:139], v180 offset:0
	ds_read_b128 v[192:195], v187 offset:0
	ds_read_b128 v[196:199], v187 offset:0x2000
	ds_read_b128 v[200:203], v180 offset:0x400
	s_waitcnt lgkmcnt(3)
	s_nop 0
	v_mfma_f32_32x32x16_bf16 v[144:159], v[128:131], v[136:139], 0
	v_mfma_f32_32x32x16_bf16 v[128:143], v[132:135], v[136:139], 0
	ds_read_b128 v[204:207], v186 offset:0
	ds_read_b128 v[208:211], v186 offset:0x2000
	ds_read_b128 v[212:215], v180 offset:0x800
	s_waitcnt lgkmcnt(3)
	v_mfma_f32_32x32x16_bf16 v[144:159], v[192:195], v[200:203], v[144:159]
	v_mfma_f32_32x32x16_bf16 v[128:143], v[196:199], v[200:203], v[128:143]
	ds_read_b128 v[192:195], v185 offset:0
	ds_read_b128 v[196:199], v185 offset:0x2000
	ds_read_b128 v[200:203], v180 offset:0xc00
	s_waitcnt lgkmcnt(3)
	v_mfma_f32_32x32x16_bf16 v[144:159], v[204:207], v[212:215], v[144:159]
	v_mfma_f32_32x32x16_bf16 v[128:143], v[208:211], v[212:215], v[128:143]
	ds_read_b128 v[204:207], v188 offset:0x80
	ds_read_b128 v[208:211], v188 offset:0x2080
	ds_read_b128 v[212:215], v180 offset:0x1000
	s_waitcnt lgkmcnt(3)
	v_mfma_f32_32x32x16_bf16 v[144:159], v[192:195], v[200:203], v[144:159]
	v_mfma_f32_32x32x16_bf16 v[128:143], v[196:199], v[200:203], v[128:143]
	ds_read_b128 v[192:195], v187 offset:0x80
	ds_read_b128 v[196:199], v187 offset:0x2080
	ds_read_b128 v[200:203], v180 offset:0x1400
	s_waitcnt lgkmcnt(3)
	v_mfma_f32_32x32x16_bf16 v[144:159], v[204:207], v[212:215], v[144:159]
	v_mfma_f32_32x32x16_bf16 v[128:143], v[208:211], v[212:215], v[128:143]
	ds_read_b128 v[204:207], v186 offset:0x80
	ds_read_b128 v[208:211], v186 offset:0x2080
	ds_read_b128 v[212:215], v180 offset:0x1800
	s_waitcnt lgkmcnt(3)
	v_mfma_f32_32x32x16_bf16 v[144:159], v[192:195], v[200:203], v[144:159]
	v_mfma_f32_32x32x16_bf16 v[128:143], v[196:199], v[200:203], v[128:143]
	ds_read_b128 v[192:195], v185 offset:0x80
	ds_read_b128 v[196:199], v185 offset:0x2080
	s_waitcnt lgkmcnt(2)
	v_mfma_f32_32x32x16_bf16 v[144:159], v[204:207], v[212:215], v[144:159]
	v_mfma_f32_32x32x16_bf16 v[128:143], v[208:211], v[212:215], v[128:143]
	s_waitcnt lgkmcnt(0)
	v_mfma_f32_32x32x16_bf16 v[144:159], v[192:195], v[166:169], v[144:159]
	v_mfma_f32_32x32x16_bf16 v[128:143], v[196:199], v[166:169], v[128:143]
	s_bitcmp0_b32 s100, 8
	s_cbranch_scc1 .Lstg_a10
	s_waitcnt vmcnt(0)
	s_waitcnt lgkmcnt(0)
	s_barrier

.LBB0_565:
	ds_read_b64_tr_b16 v[144:145], v177 offset:0x8000
	ds_read_b64_tr_b16 v[146:147], v177 offset:0x9000
	ds_read_b64_tr_b16 v[148:149], v177 offset:0xa000
	ds_read_b64_tr_b16 v[150:151], v177 offset:0xb000
	ds_read_b64_tr_b16 v[152:153], v177 offset:0xc000
	ds_read_b64_tr_b16 v[154:155], v177 offset:0xd000
	ds_read_b64_tr_b16 v[156:157], v177 offset:0xe000
	ds_read_b64_tr_b16 v[158:159], v177 offset:0xf000
	s_waitcnt lgkmcnt(6)
	s_nop 0
	v_mfma_f32_32x32x16_bf16 v[112:127], v[144:147], v[128:131], v[112:127]
	ds_read_b64_tr_b16 v[194:195], v177 offset:0x8200
	ds_read_b64_tr_b16 v[196:197], v177 offset:0x9200
	s_waitcnt lgkmcnt(6)
	v_mfma_f32_32x32x16_bf16 v[112:127], v[148:151], v[132:135], v[112:127]
	ds_read_b64_tr_b16 v[198:199], v177 offset:0xa200
	ds_read_b64_tr_b16 v[200:201], v177 offset:0xb200
	s_waitcnt lgkmcnt(6)
	v_mfma_f32_32x32x16_bf16 v[112:127], v[152:155], v[136:139], v[112:127]
	ds_read_b64_tr_b16 v[202:203], v177 offset:0xc200
	ds_read_b64_tr_b16 v[204:205], v177 offset:0xd200
	s_waitcnt lgkmcnt(6)
	v_mfma_f32_32x32x16_bf16 v[112:127], v[156:159], v[140:143], v[112:127]
	ds_read_b64_tr_b16 v[206:207], v177 offset:0xe200
	ds_read_b64_tr_b16 v[208:209], v177 offset:0xf200
	s_waitcnt lgkmcnt(6)
	v_mfma_f32_32x32x16_bf16 v[80:95], v[194:197], v[128:131], v[80:95]
	ds_read_b64_tr_b16 v[144:145], v177 offset:0x8400
	ds_read_b64_tr_b16 v[146:147], v177 offset:0x9400
	s_waitcnt lgkmcnt(6)
	v_mfma_f32_32x32x16_bf16 v[80:95], v[198:201], v[132:135], v[80:95]
	ds_read_b64_tr_b16 v[148:149], v177 offset:0xa400
	ds_read_b64_tr_b16 v[150:151], v177 offset:0xb400
	s_waitcnt lgkmcnt(6)
	v_mfma_f32_32x32x16_bf16 v[80:95], v[202:205], v[136:139], v[80:95]
	ds_read_b64_tr_b16 v[152:153], v177 offset:0xc400
	ds_read_b64_tr_b16 v[154:155], v177 offset:0xd400
	s_waitcnt lgkmcnt(6)
	v_mfma_f32_32x32x16_bf16 v[80:95], v[206:209], v[140:143], v[80:95]
	ds_read_b64_tr_b16 v[156:157], v177 offset:0xe400
	ds_read_b64_tr_b16 v[158:159], v177 offset:0xf400
	s_waitcnt lgkmcnt(6)
	v_mfma_f32_32x32x16_bf16 v[96:111], v[144:147], v[128:131], v[96:111]
	ds_read_b64_tr_b16 v[194:195], v177 offset:0x8600
	ds_read_b64_tr_b16 v[196:197], v177 offset:0x9600
	s_waitcnt lgkmcnt(6)
	v_mfma_f32_32x32x16_bf16 v[96:111], v[148:151], v[132:135], v[96:111]
	ds_read_b64_tr_b16 v[198:199], v177 offset:0xa600
	ds_read_b64_tr_b16 v[200:201], v177 offset:0xb600
	s_waitcnt lgkmcnt(6)
	v_mfma_f32_32x32x16_bf16 v[96:111], v[152:155], v[136:139], v[96:111]
	ds_read_b64_tr_b16 v[202:203], v177 offset:0xc600
	ds_read_b64_tr_b16 v[204:205], v177 offset:0xd600
	s_waitcnt lgkmcnt(6)
	v_mfma_f32_32x32x16_bf16 v[96:111], v[156:159], v[140:143], v[96:111]
	ds_read_b64_tr_b16 v[206:207], v177 offset:0xe600
	ds_read_b64_tr_b16 v[208:209], v177 offset:0xf600
	s_waitcnt lgkmcnt(6)
	v_mfma_f32_32x32x16_bf16 v[64:79], v[194:197], v[128:131], v[64:79]
	ds_read_b64_tr_b16 v[144:145], v177 offset:0x8800
	ds_read_b64_tr_b16 v[146:147], v177 offset:0x9800
	s_waitcnt lgkmcnt(6)
	v_mfma_f32_32x32x16_bf16 v[64:79], v[198:201], v[132:135], v[64:79]
	ds_read_b64_tr_b16 v[148:149], v177 offset:0xa800
	ds_read_b64_tr_b16 v[150:151], v177 offset:0xb800
	s_waitcnt lgkmcnt(6)
	v_mfma_f32_32x32x16_bf16 v[64:79], v[202:205], v[136:139], v[64:79]
	ds_read_b64_tr_b16 v[152:153], v177 offset:0xc800
	ds_read_b64_tr_b16 v[154:155], v177 offset:0xd800
	s_waitcnt lgkmcnt(6)
	v_mfma_f32_32x32x16_bf16 v[64:79], v[206:209], v[140:143], v[64:79]
	ds_read_b64_tr_b16 v[156:157], v177 offset:0xe800
	ds_read_b64_tr_b16 v[158:159], v177 offset:0xf800
	s_waitcnt lgkmcnt(6)
	v_mfma_f32_32x32x16_bf16 v[48:63], v[144:147], v[128:131], v[48:63]
	ds_read_b64_tr_b16 v[194:195], v177 offset:0x8a00
	ds_read_b64_tr_b16 v[196:197], v177 offset:0x9a00
	s_waitcnt lgkmcnt(6)
	v_mfma_f32_32x32x16_bf16 v[48:63], v[148:151], v[132:135], v[48:63]
	ds_read_b64_tr_b16 v[198:199], v177 offset:0xaa00
	ds_read_b64_tr_b16 v[200:201], v177 offset:0xba00
	s_waitcnt lgkmcnt(6)
	v_mfma_f32_32x32x16_bf16 v[48:63], v[152:155], v[136:139], v[48:63]
	ds_read_b64_tr_b16 v[202:203], v177 offset:0xca00
	ds_read_b64_tr_b16 v[204:205], v177 offset:0xda00
	s_waitcnt lgkmcnt(6)
	v_mfma_f32_32x32x16_bf16 v[48:63], v[156:159], v[140:143], v[48:63]
	ds_read_b64_tr_b16 v[206:207], v177 offset:0xea00
	ds_read_b64_tr_b16 v[208:209], v177 offset:0xfa00
	s_waitcnt lgkmcnt(6)
	v_mfma_f32_32x32x16_bf16 v[32:47], v[194:197], v[128:131], v[32:47]
	ds_read_b64_tr_b16 v[144:145], v177 offset:0x8c00
	ds_read_b64_tr_b16 v[146:147], v177 offset:0x9c00
	s_waitcnt lgkmcnt(6)
	v_mfma_f32_32x32x16_bf16 v[32:47], v[198:201], v[132:135], v[32:47]
	ds_read_b64_tr_b16 v[148:149], v177 offset:0xac00
	ds_read_b64_tr_b16 v[150:151], v177 offset:0xbc00
	s_waitcnt lgkmcnt(6)
	v_mfma_f32_32x32x16_bf16 v[32:47], v[202:205], v[136:139], v[32:47]
	ds_read_b64_tr_b16 v[152:153], v177 offset:0xcc00
	ds_read_b64_tr_b16 v[154:155], v177 offset:0xdc00
	s_waitcnt lgkmcnt(6)
	v_mfma_f32_32x32x16_bf16 v[32:47], v[206:209], v[140:143], v[32:47]
	ds_read_b64_tr_b16 v[156:157], v177 offset:0xec00
	ds_read_b64_tr_b16 v[158:159], v177 offset:0xfc00
	s_waitcnt lgkmcnt(6)
	v_mfma_f32_32x32x16_bf16 v[16:31], v[144:147], v[128:131], v[16:31]
	ds_read_b64_tr_b16 v[194:195], v177 offset:0x8e00
	ds_read_b64_tr_b16 v[196:197], v177 offset:0x9e00
	s_waitcnt lgkmcnt(6)
	v_mfma_f32_32x32x16_bf16 v[16:31], v[148:151], v[132:135], v[16:31]
	ds_read_b64_tr_b16 v[198:199], v177 offset:0xae00
	ds_read_b64_tr_b16 v[200:201], v177 offset:0xbe00
	s_waitcnt lgkmcnt(6)
	v_mfma_f32_32x32x16_bf16 v[16:31], v[152:155], v[136:139], v[16:31]
	ds_read_b64_tr_b16 v[202:203], v177 offset:0xce00
	ds_read_b64_tr_b16 v[204:205], v177 offset:0xde00
	s_waitcnt lgkmcnt(6)
	v_mfma_f32_32x32x16_bf16 v[16:31], v[156:159], v[140:143], v[16:31]
	ds_read_b64_tr_b16 v[206:207], v177 offset:0xee00
	ds_read_b64_tr_b16 v[208:209], v177 offset:0xfe00
	s_waitcnt lgkmcnt(6)
	v_mfma_f32_32x32x16_bf16 v[0:15], v[194:197], v[128:131], v[0:15]
	s_waitcnt lgkmcnt(4)
	v_mfma_f32_32x32x16_bf16 v[0:15], v[198:201], v[132:135], v[0:15]
	s_waitcnt lgkmcnt(2)
	v_mfma_f32_32x32x16_bf16 v[0:15], v[202:205], v[136:139], v[0:15]
	s_waitcnt lgkmcnt(0)
	v_mfma_f32_32x32x16_bf16 v[0:15], v[206:209], v[140:143], v[0:15]
	ds_read_b128 v[128:131], v181 offset:0
	ds_read_b128 v[132:135], v181 offset:0x2000
	ds_read_b128 v[136:139], v180 offset:0
	ds_read_b128 v[194:197], v182 offset:0
	ds_read_b128 v[198:201], v182 offset:0x2000
	ds_read_b128 v[202:205], v180 offset:0x400
	s_waitcnt lgkmcnt(3)
	s_nop 0
	v_mfma_f32_32x32x16_bf16 v[144:159], v[128:131], v[136:139], 0
	v_mfma_f32_32x32x16_bf16 v[128:143], v[132:135], v[136:139], 0
	ds_read_b128 v[206:209], v183 offset:0
	ds_read_b128 v[210:213], v183 offset:0x2000
	ds_read_b128 v[214:217], v180 offset:0x800
	s_waitcnt lgkmcnt(3)
	v_mfma_f32_32x32x16_bf16 v[144:159], v[194:197], v[202:205], v[144:159]
	v_mfma_f32_32x32x16_bf16 v[128:143], v[198:201], v[202:205], v[128:143]
	ds_read_b128 v[194:197], v184 offset:0
	ds_read_b128 v[198:201], v184 offset:0x2000
	ds_read_b128 v[202:205], v180 offset:0xc00
	s_waitcnt lgkmcnt(3)
	v_mfma_f32_32x32x16_bf16 v[144:159], v[206:209], v[214:217], v[144:159]
	v_mfma_f32_32x32x16_bf16 v[128:143], v[210:213], v[214:217], v[128:143]
	ds_read_b128 v[206:209], v181 offset:0x80
	ds_read_b128 v[210:213], v181 offset:0x2080
	ds_read_b128 v[214:217], v180 offset:0x1000
	s_waitcnt lgkmcnt(3)
	v_mfma_f32_32x32x16_bf16 v[144:159], v[194:197], v[202:205], v[144:159]
	v_mfma_f32_32x32x16_bf16 v[128:143], v[198:201], v[202:205], v[128:143]
	ds_read_b128 v[194:197], v182 offset:0x80
	ds_read_b128 v[198:201], v182 offset:0x2080
	ds_read_b128 v[202:205], v180 offset:0x1400
	s_waitcnt lgkmcnt(3)
	v_mfma_f32_32x32x16_bf16 v[144:159], v[206:209], v[214:217], v[144:159]
	v_mfma_f32_32x32x16_bf16 v[128:143], v[210:213], v[214:217], v[128:143]
	ds_read_b128 v[206:209], v183 offset:0x80
	ds_read_b128 v[210:213], v183 offset:0x2080
	ds_read_b128 v[214:217], v180 offset:0x1800
	s_waitcnt lgkmcnt(3)
	v_mfma_f32_32x32x16_bf16 v[144:159], v[194:197], v[202:205], v[144:159]
	v_mfma_f32_32x32x16_bf16 v[128:143], v[198:201], v[202:205], v[128:143]
	ds_read_b128 v[194:197], v184 offset:0x80
	ds_read_b128 v[198:201], v184 offset:0x2080
	s_waitcnt lgkmcnt(2)
	v_mfma_f32_32x32x16_bf16 v[144:159], v[206:209], v[214:217], v[144:159]
	v_mfma_f32_32x32x16_bf16 v[128:143], v[210:213], v[214:217], v[128:143]
	s_waitcnt lgkmcnt(0)
	v_mfma_f32_32x32x16_bf16 v[144:159], v[194:197], v[166:169], v[144:159]
	v_mfma_f32_32x32x16_bf16 v[128:143], v[198:201], v[166:169], v[128:143]
	s_bitcmp0_b32 s100, 8
	s_cbranch_scc1 .Lstg_a11
	s_waitcnt vmcnt(0)
	s_waitcnt lgkmcnt(0)
	s_barrier

.LBB0_580:
	ds_read_b64_tr_b16 v[144:145], v177 offset:0
	ds_read_b64_tr_b16 v[146:147], v177 offset:0x1000
	ds_read_b64_tr_b16 v[148:149], v177 offset:0x2000
	ds_read_b64_tr_b16 v[150:151], v177 offset:0x3000
	ds_read_b64_tr_b16 v[152:153], v177 offset:0x4000
	ds_read_b64_tr_b16 v[154:155], v177 offset:0x5000
	ds_read_b64_tr_b16 v[156:157], v177 offset:0x6000
	ds_read_b64_tr_b16 v[158:159], v177 offset:0x7000
	s_waitcnt lgkmcnt(6)
	s_nop 0
	v_mfma_f32_32x32x16_bf16 v[112:127], v[144:147], v[128:131], v[112:127]
	ds_read_b64_tr_b16 v[192:193], v177 offset:0x200
	ds_read_b64_tr_b16 v[194:195], v177 offset:0x1200
	s_waitcnt lgkmcnt(6)
	v_mfma_f32_32x32x16_bf16 v[112:127], v[148:151], v[132:135], v[112:127]
	ds_read_b64_tr_b16 v[196:197], v177 offset:0x2200
	ds_read_b64_tr_b16 v[198:199], v177 offset:0x3200
	s_waitcnt lgkmcnt(6)
	v_mfma_f32_32x32x16_bf16 v[112:127], v[152:155], v[136:139], v[112:127]
	ds_read_b64_tr_b16 v[200:201], v177 offset:0x4200
	ds_read_b64_tr_b16 v[202:203], v177 offset:0x5200
	s_waitcnt lgkmcnt(6)
	v_mfma_f32_32x32x16_bf16 v[112:127], v[156:159], v[140:143], v[112:127]
	ds_read_b64_tr_b16 v[204:205], v177 offset:0x6200
	ds_read_b64_tr_b16 v[206:207], v177 offset:0x7200
	s_waitcnt lgkmcnt(6)
	v_mfma_f32_32x32x16_bf16 v[80:95], v[192:195], v[128:131], v[80:95]
	ds_read_b64_tr_b16 v[144:145], v177 offset:0x400
	ds_read_b64_tr_b16 v[146:147], v177 offset:0x1400
	s_waitcnt lgkmcnt(6)
	v_mfma_f32_32x32x16_bf16 v[80:95], v[196:199], v[132:135], v[80:95]
	ds_read_b64_tr_b16 v[148:149], v177 offset:0x2400
	ds_read_b64_tr_b16 v[150:151], v177 offset:0x3400
	s_waitcnt lgkmcnt(6)
	v_mfma_f32_32x32x16_bf16 v[80:95], v[200:203], v[136:139], v[80:95]
	ds_read_b64_tr_b16 v[152:153], v177 offset:0x4400
	ds_read_b64_tr_b16 v[154:155], v177 offset:0x5400
	s_waitcnt lgkmcnt(6)
	v_mfma_f32_32x32x16_bf16 v[80:95], v[204:207], v[140:143], v[80:95]
	ds_read_b64_tr_b16 v[156:157], v177 offset:0x6400
	ds_read_b64_tr_b16 v[158:159], v177 offset:0x7400
	s_waitcnt lgkmcnt(6)
	v_mfma_f32_32x32x16_bf16 v[96:111], v[144:147], v[128:131], v[96:111]
	ds_read_b64_tr_b16 v[192:193], v177 offset:0x600
	ds_read_b64_tr_b16 v[194:195], v177 offset:0x1600
	s_waitcnt lgkmcnt(6)
	v_mfma_f32_32x32x16_bf16 v[96:111], v[148:151], v[132:135], v[96:111]
	ds_read_b64_tr_b16 v[196:197], v177 offset:0x2600
	ds_read_b64_tr_b16 v[198:199], v177 offset:0x3600
	s_waitcnt lgkmcnt(6)
	v_mfma_f32_32x32x16_bf16 v[96:111], v[152:155], v[136:139], v[96:111]
	ds_read_b64_tr_b16 v[200:201], v177 offset:0x4600
	ds_read_b64_tr_b16 v[202:203], v177 offset:0x5600
	s_waitcnt lgkmcnt(6)
	v_mfma_f32_32x32x16_bf16 v[96:111], v[156:159], v[140:143], v[96:111]
	ds_read_b64_tr_b16 v[204:205], v177 offset:0x6600
	ds_read_b64_tr_b16 v[206:207], v177 offset:0x7600
	s_waitcnt lgkmcnt(6)
	v_mfma_f32_32x32x16_bf16 v[64:79], v[192:195], v[128:131], v[64:79]
	ds_read_b64_tr_b16 v[144:145], v177 offset:0x800
	ds_read_b64_tr_b16 v[146:147], v177 offset:0x1800
	s_waitcnt lgkmcnt(6)
	v_mfma_f32_32x32x16_bf16 v[64:79], v[196:199], v[132:135], v[64:79]
	ds_read_b64_tr_b16 v[148:149], v177 offset:0x2800
	ds_read_b64_tr_b16 v[150:151], v177 offset:0x3800
	s_waitcnt lgkmcnt(6)
	v_mfma_f32_32x32x16_bf16 v[64:79], v[200:203], v[136:139], v[64:79]
	ds_read_b64_tr_b16 v[152:153], v177 offset:0x4800
	ds_read_b64_tr_b16 v[154:155], v177 offset:0x5800
	s_waitcnt lgkmcnt(6)
	v_mfma_f32_32x32x16_bf16 v[64:79], v[204:207], v[140:143], v[64:79]
	ds_read_b64_tr_b16 v[156:157], v177 offset:0x6800
	ds_read_b64_tr_b16 v[158:159], v177 offset:0x7800
	s_waitcnt lgkmcnt(6)
	v_mfma_f32_32x32x16_bf16 v[48:63], v[144:147], v[128:131], v[48:63]
	ds_read_b64_tr_b16 v[192:193], v177 offset:0xa00
	ds_read_b64_tr_b16 v[194:195], v177 offset:0x1a00
	s_waitcnt lgkmcnt(6)
	v_mfma_f32_32x32x16_bf16 v[48:63], v[148:151], v[132:135], v[48:63]
	ds_read_b64_tr_b16 v[196:197], v177 offset:0x2a00
	ds_read_b64_tr_b16 v[198:199], v177 offset:0x3a00
	s_waitcnt lgkmcnt(6)
	v_mfma_f32_32x32x16_bf16 v[48:63], v[152:155], v[136:139], v[48:63]
	ds_read_b64_tr_b16 v[200:201], v177 offset:0x4a00
	ds_read_b64_tr_b16 v[202:203], v177 offset:0x5a00
	s_waitcnt lgkmcnt(6)
	v_mfma_f32_32x32x16_bf16 v[48:63], v[156:159], v[140:143], v[48:63]
	ds_read_b64_tr_b16 v[204:205], v177 offset:0x6a00
	ds_read_b64_tr_b16 v[206:207], v177 offset:0x7a00
	s_waitcnt lgkmcnt(6)
	v_mfma_f32_32x32x16_bf16 v[32:47], v[192:195], v[128:131], v[32:47]
	ds_read_b64_tr_b16 v[144:145], v177 offset:0xc00
	ds_read_b64_tr_b16 v[146:147], v177 offset:0x1c00
	s_waitcnt lgkmcnt(6)
	v_mfma_f32_32x32x16_bf16 v[32:47], v[196:199], v[132:135], v[32:47]
	ds_read_b64_tr_b16 v[148:149], v177 offset:0x2c00
	ds_read_b64_tr_b16 v[150:151], v177 offset:0x3c00
	s_waitcnt lgkmcnt(6)
	v_mfma_f32_32x32x16_bf16 v[32:47], v[200:203], v[136:139], v[32:47]
	ds_read_b64_tr_b16 v[152:153], v177 offset:0x4c00
	ds_read_b64_tr_b16 v[154:155], v177 offset:0x5c00
	s_waitcnt lgkmcnt(6)
	v_mfma_f32_32x32x16_bf16 v[32:47], v[204:207], v[140:143], v[32:47]
	ds_read_b64_tr_b16 v[156:157], v177 offset:0x6c00
	ds_read_b64_tr_b16 v[158:159], v177 offset:0x7c00
	s_waitcnt lgkmcnt(6)
	v_mfma_f32_32x32x16_bf16 v[16:31], v[144:147], v[128:131], v[16:31]
	ds_read_b64_tr_b16 v[192:193], v177 offset:0xe00
	ds_read_b64_tr_b16 v[194:195], v177 offset:0x1e00
	s_waitcnt lgkmcnt(6)
	v_mfma_f32_32x32x16_bf16 v[16:31], v[148:151], v[132:135], v[16:31]
	ds_read_b64_tr_b16 v[196:197], v177 offset:0x2e00
	ds_read_b64_tr_b16 v[198:199], v177 offset:0x3e00
	s_waitcnt lgkmcnt(6)
	v_mfma_f32_32x32x16_bf16 v[16:31], v[152:155], v[136:139], v[16:31]
	ds_read_b64_tr_b16 v[200:201], v177 offset:0x4e00
	ds_read_b64_tr_b16 v[202:203], v177 offset:0x5e00
	s_waitcnt lgkmcnt(6)
	v_mfma_f32_32x32x16_bf16 v[16:31], v[156:159], v[140:143], v[16:31]
	ds_read_b64_tr_b16 v[204:205], v177 offset:0x6e00
	ds_read_b64_tr_b16 v[206:207], v177 offset:0x7e00
	s_waitcnt lgkmcnt(6)
	v_mfma_f32_32x32x16_bf16 v[0:15], v[192:195], v[128:131], v[0:15]
	s_waitcnt lgkmcnt(4)
	v_mfma_f32_32x32x16_bf16 v[0:15], v[196:199], v[132:135], v[0:15]
	s_waitcnt lgkmcnt(2)
	v_mfma_f32_32x32x16_bf16 v[0:15], v[200:203], v[136:139], v[0:15]
	s_waitcnt lgkmcnt(0)
	v_mfma_f32_32x32x16_bf16 v[0:15], v[204:207], v[140:143], v[0:15]
	ds_read_b128 v[128:131], v188 offset:0
	ds_read_b128 v[132:135], v188 offset:0x2000
	ds_read_b128 v[136:139], v180 offset:0
	ds_read_b128 v[192:195], v187 offset:0
	ds_read_b128 v[196:199], v187 offset:0x2000
	ds_read_b128 v[200:203], v180 offset:0x400
	s_waitcnt lgkmcnt(3)
	s_nop 0
	v_mfma_f32_32x32x16_bf16 v[144:159], v[128:131], v[136:139], 0
	v_mfma_f32_32x32x16_bf16 v[128:143], v[132:135], v[136:139], 0
	ds_read_b128 v[204:207], v186 offset:0
	ds_read_b128 v[208:211], v186 offset:0x2000
	ds_read_b128 v[212:215], v180 offset:0x800
	s_waitcnt lgkmcnt(3)
	v_mfma_f32_32x32x16_bf16 v[144:159], v[192:195], v[200:203], v[144:159]
	v_mfma_f32_32x32x16_bf16 v[128:143], v[196:199], v[200:203], v[128:143]
	ds_read_b128 v[192:195], v185 offset:0
	ds_read_b128 v[196:199], v185 offset:0x2000
	ds_read_b128 v[200:203], v180 offset:0xc00
	s_waitcnt lgkmcnt(3)
	v_mfma_f32_32x32x16_bf16 v[144:159], v[204:207], v[212:215], v[144:159]
	v_mfma_f32_32x32x16_bf16 v[128:143], v[208:211], v[212:215], v[128:143]
	ds_read_b128 v[204:207], v188 offset:0x80
	ds_read_b128 v[208:211], v188 offset:0x2080
	ds_read_b128 v[212:215], v180 offset:0x1000
	s_waitcnt lgkmcnt(3)
	v_mfma_f32_32x32x16_bf16 v[144:159], v[192:195], v[200:203], v[144:159]
	v_mfma_f32_32x32x16_bf16 v[128:143], v[196:199], v[200:203], v[128:143]
	ds_read_b128 v[192:195], v187 offset:0x80
	ds_read_b128 v[196:199], v187 offset:0x2080
	ds_read_b128 v[200:203], v180 offset:0x1400
	s_waitcnt lgkmcnt(3)
	v_mfma_f32_32x32x16_bf16 v[144:159], v[204:207], v[212:215], v[144:159]
	v_mfma_f32_32x32x16_bf16 v[128:143], v[208:211], v[212:215], v[128:143]
	ds_read_b128 v[204:207], v186 offset:0x80
	ds_read_b128 v[208:211], v186 offset:0x2080
	ds_read_b128 v[186:189], v180 offset:0x1800
	s_waitcnt lgkmcnt(3)
	v_mfma_f32_32x32x16_bf16 v[144:159], v[192:195], v[200:203], v[144:159]
	v_mfma_f32_32x32x16_bf16 v[128:143], v[196:199], v[200:203], v[128:143]
	ds_read_b128 v[180:183], v185 offset:0x80
	ds_read_b128 v[192:195], v185 offset:0x2080
	s_waitcnt lgkmcnt(2)
	v_mfma_f32_32x32x16_bf16 v[144:159], v[204:207], v[186:189], v[144:159]
	v_mfma_f32_32x32x16_bf16 v[128:143], v[208:211], v[186:189], v[128:143]
	s_waitcnt lgkmcnt(0)
	v_mfma_f32_32x32x16_bf16 v[144:159], v[180:183], v[166:169], v[144:159]
	v_mfma_f32_32x32x16_bf16 v[128:143], v[192:195], v[166:169], v[128:143]
	s_bitcmp0_b32 s100, 8
	s_cbranch_scc1 .Lstg_a12
	s_waitcnt vmcnt(0)
	s_waitcnt lgkmcnt(0)
	s_barrier

.LBB0_589:
	ds_read_b64_tr_b16 v[144:145], v177 offset:0
	ds_read_b64_tr_b16 v[146:147], v177 offset:0x1000
	ds_read_b64_tr_b16 v[148:149], v177 offset:0x2000
	ds_read_b64_tr_b16 v[150:151], v177 offset:0x3000
	ds_read_b64_tr_b16 v[152:153], v177 offset:0x4000
	ds_read_b64_tr_b16 v[154:155], v177 offset:0x5000
	ds_read_b64_tr_b16 v[156:157], v177 offset:0x6000
	ds_read_b64_tr_b16 v[158:159], v177 offset:0x7000
	s_waitcnt lgkmcnt(6)
	s_nop 0
	v_mfma_f32_32x32x16_bf16 v[112:127], v[144:147], v[128:131], v[112:127]
	ds_read_b64_tr_b16 v[192:193], v177 offset:0x200
	ds_read_b64_tr_b16 v[194:195], v177 offset:0x1200
	s_waitcnt lgkmcnt(6)
	v_mfma_f32_32x32x16_bf16 v[112:127], v[148:151], v[132:135], v[112:127]
	ds_read_b64_tr_b16 v[196:197], v177 offset:0x2200
	ds_read_b64_tr_b16 v[198:199], v177 offset:0x3200
	s_waitcnt lgkmcnt(6)
	v_mfma_f32_32x32x16_bf16 v[112:127], v[152:155], v[136:139], v[112:127]
	ds_read_b64_tr_b16 v[200:201], v177 offset:0x4200
	ds_read_b64_tr_b16 v[202:203], v177 offset:0x5200
	s_waitcnt lgkmcnt(6)
	v_mfma_f32_32x32x16_bf16 v[112:127], v[156:159], v[140:143], v[112:127]
	ds_read_b64_tr_b16 v[204:205], v177 offset:0x6200
	ds_read_b64_tr_b16 v[206:207], v177 offset:0x7200
	s_waitcnt lgkmcnt(6)
	v_mfma_f32_32x32x16_bf16 v[96:111], v[192:195], v[128:131], v[96:111]
	ds_read_b64_tr_b16 v[144:145], v177 offset:0x400
	ds_read_b64_tr_b16 v[146:147], v177 offset:0x1400
	s_waitcnt lgkmcnt(6)
	v_mfma_f32_32x32x16_bf16 v[96:111], v[196:199], v[132:135], v[96:111]
	ds_read_b64_tr_b16 v[148:149], v177 offset:0x2400
	ds_read_b64_tr_b16 v[150:151], v177 offset:0x3400
	s_waitcnt lgkmcnt(6)
	v_mfma_f32_32x32x16_bf16 v[96:111], v[200:203], v[136:139], v[96:111]
	ds_read_b64_tr_b16 v[152:153], v177 offset:0x4400
	ds_read_b64_tr_b16 v[154:155], v177 offset:0x5400
	s_waitcnt lgkmcnt(6)
	v_mfma_f32_32x32x16_bf16 v[96:111], v[204:207], v[140:143], v[96:111]
	ds_read_b64_tr_b16 v[156:157], v177 offset:0x6400
	ds_read_b64_tr_b16 v[158:159], v177 offset:0x7400
	s_waitcnt lgkmcnt(6)
	v_mfma_f32_32x32x16_bf16 v[80:95], v[144:147], v[128:131], v[80:95]
	ds_read_b64_tr_b16 v[192:193], v177 offset:0x600
	ds_read_b64_tr_b16 v[194:195], v177 offset:0x1600
	s_waitcnt lgkmcnt(6)
	v_mfma_f32_32x32x16_bf16 v[80:95], v[148:151], v[132:135], v[80:95]
	ds_read_b64_tr_b16 v[196:197], v177 offset:0x2600
	ds_read_b64_tr_b16 v[198:199], v177 offset:0x3600
	s_waitcnt lgkmcnt(6)
	v_mfma_f32_32x32x16_bf16 v[80:95], v[152:155], v[136:139], v[80:95]
	ds_read_b64_tr_b16 v[200:201], v177 offset:0x4600
	ds_read_b64_tr_b16 v[202:203], v177 offset:0x5600
	s_waitcnt lgkmcnt(6)
	v_mfma_f32_32x32x16_bf16 v[80:95], v[156:159], v[140:143], v[80:95]
	ds_read_b64_tr_b16 v[204:205], v177 offset:0x6600
	ds_read_b64_tr_b16 v[206:207], v177 offset:0x7600
	s_waitcnt lgkmcnt(6)
	v_mfma_f32_32x32x16_bf16 v[64:79], v[192:195], v[128:131], v[64:79]
	ds_read_b64_tr_b16 v[144:145], v177 offset:0x800
	ds_read_b64_tr_b16 v[146:147], v177 offset:0x1800
	s_waitcnt lgkmcnt(6)
	v_mfma_f32_32x32x16_bf16 v[64:79], v[196:199], v[132:135], v[64:79]
	ds_read_b64_tr_b16 v[148:149], v177 offset:0x2800
	ds_read_b64_tr_b16 v[150:151], v177 offset:0x3800
	s_waitcnt lgkmcnt(6)
	v_mfma_f32_32x32x16_bf16 v[64:79], v[200:203], v[136:139], v[64:79]
	ds_read_b64_tr_b16 v[152:153], v177 offset:0x4800
	ds_read_b64_tr_b16 v[154:155], v177 offset:0x5800
	s_waitcnt lgkmcnt(6)
	v_mfma_f32_32x32x16_bf16 v[64:79], v[204:207], v[140:143], v[64:79]
	ds_read_b64_tr_b16 v[156:157], v177 offset:0x6800
	ds_read_b64_tr_b16 v[158:159], v177 offset:0x7800
	s_waitcnt lgkmcnt(6)
	v_mfma_f32_32x32x16_bf16 v[48:63], v[144:147], v[128:131], v[48:63]
	ds_read_b64_tr_b16 v[192:193], v177 offset:0xa00
	ds_read_b64_tr_b16 v[194:195], v177 offset:0x1a00
	s_waitcnt lgkmcnt(6)
	v_mfma_f32_32x32x16_bf16 v[48:63], v[148:151], v[132:135], v[48:63]
	ds_read_b64_tr_b16 v[196:197], v177 offset:0x2a00
	ds_read_b64_tr_b16 v[198:199], v177 offset:0x3a00
	s_waitcnt lgkmcnt(6)
	v_mfma_f32_32x32x16_bf16 v[48:63], v[152:155], v[136:139], v[48:63]
	ds_read_b64_tr_b16 v[200:201], v177 offset:0x4a00
	ds_read_b64_tr_b16 v[202:203], v177 offset:0x5a00
	s_waitcnt lgkmcnt(6)
	v_mfma_f32_32x32x16_bf16 v[48:63], v[156:159], v[140:143], v[48:63]
	ds_read_b64_tr_b16 v[204:205], v177 offset:0x6a00
	ds_read_b64_tr_b16 v[206:207], v177 offset:0x7a00
	s_waitcnt lgkmcnt(6)
	v_mfma_f32_32x32x16_bf16 v[32:47], v[192:195], v[128:131], v[32:47]
	ds_read_b64_tr_b16 v[144:145], v177 offset:0xc00
	ds_read_b64_tr_b16 v[146:147], v177 offset:0x1c00
	s_waitcnt lgkmcnt(6)
	v_mfma_f32_32x32x16_bf16 v[32:47], v[196:199], v[132:135], v[32:47]
	ds_read_b64_tr_b16 v[148:149], v177 offset:0x2c00
	ds_read_b64_tr_b16 v[150:151], v177 offset:0x3c00
	s_waitcnt lgkmcnt(6)
	v_mfma_f32_32x32x16_bf16 v[32:47], v[200:203], v[136:139], v[32:47]
	ds_read_b64_tr_b16 v[152:153], v177 offset:0x4c00
	ds_read_b64_tr_b16 v[154:155], v177 offset:0x5c00
	s_waitcnt lgkmcnt(6)
	v_mfma_f32_32x32x16_bf16 v[32:47], v[204:207], v[140:143], v[32:47]
	ds_read_b64_tr_b16 v[156:157], v177 offset:0x6c00
	ds_read_b64_tr_b16 v[158:159], v177 offset:0x7c00
	s_waitcnt lgkmcnt(6)
	v_mfma_f32_32x32x16_bf16 v[16:31], v[144:147], v[128:131], v[16:31]
	ds_read_b64_tr_b16 v[192:193], v177 offset:0xe00
	ds_read_b64_tr_b16 v[194:195], v177 offset:0x1e00
	s_waitcnt lgkmcnt(6)
	v_mfma_f32_32x32x16_bf16 v[16:31], v[148:151], v[132:135], v[16:31]
	ds_read_b64_tr_b16 v[196:197], v177 offset:0x2e00
	ds_read_b64_tr_b16 v[198:199], v177 offset:0x3e00
	s_waitcnt lgkmcnt(6)
	v_mfma_f32_32x32x16_bf16 v[16:31], v[152:155], v[136:139], v[16:31]
	ds_read_b64_tr_b16 v[200:201], v177 offset:0x4e00
	ds_read_b64_tr_b16 v[202:203], v177 offset:0x5e00
	s_waitcnt lgkmcnt(6)
	v_mfma_f32_32x32x16_bf16 v[16:31], v[156:159], v[140:143], v[16:31]
	ds_read_b64_tr_b16 v[204:205], v177 offset:0x6e00
	ds_read_b64_tr_b16 v[206:207], v177 offset:0x7e00
	s_waitcnt lgkmcnt(6)
	v_mfma_f32_32x32x16_bf16 v[0:15], v[192:195], v[128:131], v[0:15]
	s_waitcnt lgkmcnt(4)
	v_mfma_f32_32x32x16_bf16 v[0:15], v[196:199], v[132:135], v[0:15]
	s_waitcnt lgkmcnt(2)
	v_mfma_f32_32x32x16_bf16 v[0:15], v[200:203], v[136:139], v[0:15]
	s_waitcnt lgkmcnt(0)
	v_mfma_f32_32x32x16_bf16 v[0:15], v[204:207], v[140:143], v[0:15]
	ds_read_b128 v[128:131], v188 offset:0
	ds_read_b128 v[132:135], v188 offset:0x2000
	ds_read_b128 v[136:139], v180 offset:0
	ds_read_b128 v[192:195], v187 offset:0
	ds_read_b128 v[196:199], v187 offset:0x2000
	ds_read_b128 v[200:203], v180 offset:0x400
	s_waitcnt lgkmcnt(3)
	s_nop 0
	v_mfma_f32_32x32x16_bf16 v[144:159], v[128:131], v[136:139], 0
	v_mfma_f32_32x32x16_bf16 v[128:143], v[132:135], v[136:139], 0
	ds_read_b128 v[204:207], v186 offset:0
	ds_read_b128 v[208:211], v186 offset:0x2000
	ds_read_b128 v[212:215], v180 offset:0x800
	s_waitcnt lgkmcnt(3)
	v_mfma_f32_32x32x16_bf16 v[144:159], v[192:195], v[200:203], v[144:159]
	v_mfma_f32_32x32x16_bf16 v[128:143], v[196:199], v[200:203], v[128:143]
	ds_read_b128 v[192:195], v185 offset:0
	ds_read_b128 v[196:199], v185 offset:0x2000
	ds_read_b128 v[200:203], v180 offset:0xc00
	s_waitcnt lgkmcnt(3)
	v_mfma_f32_32x32x16_bf16 v[144:159], v[204:207], v[212:215], v[144:159]
	v_mfma_f32_32x32x16_bf16 v[128:143], v[208:211], v[212:215], v[128:143]
	ds_read_b128 v[204:207], v188 offset:0x80
	ds_read_b128 v[208:211], v188 offset:0x2080
	ds_read_b128 v[212:215], v180 offset:0x1000
	s_waitcnt lgkmcnt(3)
	v_mfma_f32_32x32x16_bf16 v[144:159], v[192:195], v[200:203], v[144:159]
	v_mfma_f32_32x32x16_bf16 v[128:143], v[196:199], v[200:203], v[128:143]
	ds_read_b128 v[192:195], v187 offset:0x80
	ds_read_b128 v[196:199], v187 offset:0x2080
	ds_read_b128 v[200:203], v180 offset:0x1400
	s_waitcnt lgkmcnt(3)
	v_mfma_f32_32x32x16_bf16 v[144:159], v[204:207], v[212:215], v[144:159]
	v_mfma_f32_32x32x16_bf16 v[128:143], v[208:211], v[212:215], v[128:143]
	ds_read_b128 v[204:207], v186 offset:0x80
	ds_read_b128 v[208:211], v186 offset:0x2080
	ds_read_b128 v[212:215], v180 offset:0x1800
	s_waitcnt lgkmcnt(3)
	v_mfma_f32_32x32x16_bf16 v[144:159], v[192:195], v[200:203], v[144:159]
	v_mfma_f32_32x32x16_bf16 v[128:143], v[196:199], v[200:203], v[128:143]
	ds_read_b128 v[192:195], v185 offset:0x80
	ds_read_b128 v[196:199], v185 offset:0x2080
	s_waitcnt lgkmcnt(2)
	v_mfma_f32_32x32x16_bf16 v[144:159], v[204:207], v[212:215], v[144:159]
	v_mfma_f32_32x32x16_bf16 v[128:143], v[208:211], v[212:215], v[128:143]
	s_waitcnt lgkmcnt(0)
	v_mfma_f32_32x32x16_bf16 v[144:159], v[192:195], v[166:169], v[144:159]
	v_mfma_f32_32x32x16_bf16 v[128:143], v[196:199], v[166:169], v[128:143]
	s_bitcmp0_b32 s100, 8
	s_cbranch_scc1 .Lstg_a18
	s_waitcnt vmcnt(0)
	s_waitcnt lgkmcnt(0)
	s_barrier

.LBB0_597:
	ds_read_b64_tr_b16 v[144:145], v177 offset:0x8000
	ds_read_b64_tr_b16 v[146:147], v177 offset:0x9000
	ds_read_b64_tr_b16 v[148:149], v177 offset:0xa000
	ds_read_b64_tr_b16 v[150:151], v177 offset:0xb000
	ds_read_b64_tr_b16 v[152:153], v177 offset:0xc000
	ds_read_b64_tr_b16 v[154:155], v177 offset:0xd000
	ds_read_b64_tr_b16 v[156:157], v177 offset:0xe000
	ds_read_b64_tr_b16 v[158:159], v177 offset:0xf000
	s_waitcnt lgkmcnt(6)
	s_nop 0
	v_mfma_f32_32x32x16_bf16 v[112:127], v[144:147], v[128:131], v[112:127]
	ds_read_b64_tr_b16 v[194:195], v177 offset:0x8200
	ds_read_b64_tr_b16 v[196:197], v177 offset:0x9200
	s_waitcnt lgkmcnt(6)
	v_mfma_f32_32x32x16_bf16 v[112:127], v[148:151], v[132:135], v[112:127]
	ds_read_b64_tr_b16 v[198:199], v177 offset:0xa200
	ds_read_b64_tr_b16 v[200:201], v177 offset:0xb200
	s_waitcnt lgkmcnt(6)
	v_mfma_f32_32x32x16_bf16 v[112:127], v[152:155], v[136:139], v[112:127]
	ds_read_b64_tr_b16 v[202:203], v177 offset:0xc200
	ds_read_b64_tr_b16 v[204:205], v177 offset:0xd200
	s_waitcnt lgkmcnt(6)
	v_mfma_f32_32x32x16_bf16 v[112:127], v[156:159], v[140:143], v[112:127]
	ds_read_b64_tr_b16 v[206:207], v177 offset:0xe200
	ds_read_b64_tr_b16 v[208:209], v177 offset:0xf200
	s_waitcnt lgkmcnt(6)
	v_mfma_f32_32x32x16_bf16 v[96:111], v[194:197], v[128:131], v[96:111]
	ds_read_b64_tr_b16 v[144:145], v177 offset:0x8400
	ds_read_b64_tr_b16 v[146:147], v177 offset:0x9400
	s_waitcnt lgkmcnt(6)
	v_mfma_f32_32x32x16_bf16 v[96:111], v[198:201], v[132:135], v[96:111]
	ds_read_b64_tr_b16 v[148:149], v177 offset:0xa400
	ds_read_b64_tr_b16 v[150:151], v177 offset:0xb400
	s_waitcnt lgkmcnt(6)
	v_mfma_f32_32x32x16_bf16 v[96:111], v[202:205], v[136:139], v[96:111]
	ds_read_b64_tr_b16 v[152:153], v177 offset:0xc400
	ds_read_b64_tr_b16 v[154:155], v177 offset:0xd400
	s_waitcnt lgkmcnt(6)
	v_mfma_f32_32x32x16_bf16 v[96:111], v[206:209], v[140:143], v[96:111]
	ds_read_b64_tr_b16 v[156:157], v177 offset:0xe400
	ds_read_b64_tr_b16 v[158:159], v177 offset:0xf400
	s_waitcnt lgkmcnt(6)
	v_mfma_f32_32x32x16_bf16 v[80:95], v[144:147], v[128:131], v[80:95]
	ds_read_b64_tr_b16 v[194:195], v177 offset:0x8600
	ds_read_b64_tr_b16 v[196:197], v177 offset:0x9600
	s_waitcnt lgkmcnt(6)
	v_mfma_f32_32x32x16_bf16 v[80:95], v[148:151], v[132:135], v[80:95]
	ds_read_b64_tr_b16 v[198:199], v177 offset:0xa600
	ds_read_b64_tr_b16 v[200:201], v177 offset:0xb600
	s_waitcnt lgkmcnt(6)
	v_mfma_f32_32x32x16_bf16 v[80:95], v[152:155], v[136:139], v[80:95]
	ds_read_b64_tr_b16 v[202:203], v177 offset:0xc600
	ds_read_b64_tr_b16 v[204:205], v177 offset:0xd600
	s_waitcnt lgkmcnt(6)
	v_mfma_f32_32x32x16_bf16 v[80:95], v[156:159], v[140:143], v[80:95]
	ds_read_b64_tr_b16 v[206:207], v177 offset:0xe600
	ds_read_b64_tr_b16 v[208:209], v177 offset:0xf600
	s_waitcnt lgkmcnt(6)
	v_mfma_f32_32x32x16_bf16 v[64:79], v[194:197], v[128:131], v[64:79]
	ds_read_b64_tr_b16 v[144:145], v177 offset:0x8800
	ds_read_b64_tr_b16 v[146:147], v177 offset:0x9800
	s_waitcnt lgkmcnt(6)
	v_mfma_f32_32x32x16_bf16 v[64:79], v[198:201], v[132:135], v[64:79]
	ds_read_b64_tr_b16 v[148:149], v177 offset:0xa800
	ds_read_b64_tr_b16 v[150:151], v177 offset:0xb800
	s_waitcnt lgkmcnt(6)
	v_mfma_f32_32x32x16_bf16 v[64:79], v[202:205], v[136:139], v[64:79]
	ds_read_b64_tr_b16 v[152:153], v177 offset:0xc800
	ds_read_b64_tr_b16 v[154:155], v177 offset:0xd800
	s_waitcnt lgkmcnt(6)
	v_mfma_f32_32x32x16_bf16 v[64:79], v[206:209], v[140:143], v[64:79]
	ds_read_b64_tr_b16 v[156:157], v177 offset:0xe800
	ds_read_b64_tr_b16 v[158:159], v177 offset:0xf800
	s_waitcnt lgkmcnt(6)
	v_mfma_f32_32x32x16_bf16 v[48:63], v[144:147], v[128:131], v[48:63]
	ds_read_b64_tr_b16 v[194:195], v177 offset:0x8a00
	ds_read_b64_tr_b16 v[196:197], v177 offset:0x9a00
	s_waitcnt lgkmcnt(6)
	v_mfma_f32_32x32x16_bf16 v[48:63], v[148:151], v[132:135], v[48:63]
	ds_read_b64_tr_b16 v[198:199], v177 offset:0xaa00
	ds_read_b64_tr_b16 v[200:201], v177 offset:0xba00
	s_waitcnt lgkmcnt(6)
	v_mfma_f32_32x32x16_bf16 v[48:63], v[152:155], v[136:139], v[48:63]
	ds_read_b64_tr_b16 v[202:203], v177 offset:0xca00
	ds_read_b64_tr_b16 v[204:205], v177 offset:0xda00
	s_waitcnt lgkmcnt(6)
	v_mfma_f32_32x32x16_bf16 v[48:63], v[156:159], v[140:143], v[48:63]
	ds_read_b64_tr_b16 v[206:207], v177 offset:0xea00
	ds_read_b64_tr_b16 v[208:209], v177 offset:0xfa00
	s_waitcnt lgkmcnt(6)
	v_mfma_f32_32x32x16_bf16 v[32:47], v[194:197], v[128:131], v[32:47]
	ds_read_b64_tr_b16 v[144:145], v177 offset:0x8c00
	ds_read_b64_tr_b16 v[146:147], v177 offset:0x9c00
	s_waitcnt lgkmcnt(6)
	v_mfma_f32_32x32x16_bf16 v[32:47], v[198:201], v[132:135], v[32:47]
	ds_read_b64_tr_b16 v[148:149], v177 offset:0xac00
	ds_read_b64_tr_b16 v[150:151], v177 offset:0xbc00
	s_waitcnt lgkmcnt(6)
	v_mfma_f32_32x32x16_bf16 v[32:47], v[202:205], v[136:139], v[32:47]
	ds_read_b64_tr_b16 v[152:153], v177 offset:0xcc00
	ds_read_b64_tr_b16 v[154:155], v177 offset:0xdc00
	s_waitcnt lgkmcnt(6)
	v_mfma_f32_32x32x16_bf16 v[32:47], v[206:209], v[140:143], v[32:47]
	ds_read_b64_tr_b16 v[156:157], v177 offset:0xec00
	ds_read_b64_tr_b16 v[158:159], v177 offset:0xfc00
	s_waitcnt lgkmcnt(6)
	v_mfma_f32_32x32x16_bf16 v[16:31], v[144:147], v[128:131], v[16:31]
	ds_read_b64_tr_b16 v[194:195], v177 offset:0x8e00
	ds_read_b64_tr_b16 v[196:197], v177 offset:0x9e00
	s_waitcnt lgkmcnt(6)
	v_mfma_f32_32x32x16_bf16 v[16:31], v[148:151], v[132:135], v[16:31]
	ds_read_b64_tr_b16 v[198:199], v177 offset:0xae00
	ds_read_b64_tr_b16 v[200:201], v177 offset:0xbe00
	s_waitcnt lgkmcnt(6)
	v_mfma_f32_32x32x16_bf16 v[16:31], v[152:155], v[136:139], v[16:31]
	ds_read_b64_tr_b16 v[202:203], v177 offset:0xce00
	ds_read_b64_tr_b16 v[204:205], v177 offset:0xde00
	s_waitcnt lgkmcnt(6)
	v_mfma_f32_32x32x16_bf16 v[16:31], v[156:159], v[140:143], v[16:31]
	ds_read_b64_tr_b16 v[206:207], v177 offset:0xee00
	ds_read_b64_tr_b16 v[208:209], v177 offset:0xfe00
	s_waitcnt lgkmcnt(6)
	v_mfma_f32_32x32x16_bf16 v[0:15], v[194:197], v[128:131], v[0:15]
	s_waitcnt lgkmcnt(4)
	v_mfma_f32_32x32x16_bf16 v[0:15], v[198:201], v[132:135], v[0:15]
	s_waitcnt lgkmcnt(2)
	v_mfma_f32_32x32x16_bf16 v[0:15], v[202:205], v[136:139], v[0:15]
	s_waitcnt lgkmcnt(0)
	v_mfma_f32_32x32x16_bf16 v[0:15], v[206:209], v[140:143], v[0:15]
	ds_read_b128 v[128:131], v181 offset:0
	ds_read_b128 v[132:135], v181 offset:0x2000
	ds_read_b128 v[136:139], v180 offset:0
	ds_read_b128 v[194:197], v182 offset:0
	ds_read_b128 v[198:201], v182 offset:0x2000
	ds_read_b128 v[202:205], v180 offset:0x400
	s_waitcnt lgkmcnt(3)
	s_nop 0
	v_mfma_f32_32x32x16_bf16 v[144:159], v[128:131], v[136:139], 0
	v_mfma_f32_32x32x16_bf16 v[128:143], v[132:135], v[136:139], 0
	ds_read_b128 v[206:209], v183 offset:0
	ds_read_b128 v[210:213], v183 offset:0x2000
	ds_read_b128 v[214:217], v180 offset:0x800
	s_waitcnt lgkmcnt(3)
	v_mfma_f32_32x32x16_bf16 v[144:159], v[194:197], v[202:205], v[144:159]
	v_mfma_f32_32x32x16_bf16 v[128:143], v[198:201], v[202:205], v[128:143]
	ds_read_b128 v[194:197], v184 offset:0
	ds_read_b128 v[198:201], v184 offset:0x2000
	ds_read_b128 v[202:205], v180 offset:0xc00
	s_waitcnt lgkmcnt(3)
	v_mfma_f32_32x32x16_bf16 v[144:159], v[206:209], v[214:217], v[144:159]
	v_mfma_f32_32x32x16_bf16 v[128:143], v[210:213], v[214:217], v[128:143]
	ds_read_b128 v[206:209], v181 offset:0x80
	ds_read_b128 v[210:213], v181 offset:0x2080
	ds_read_b128 v[214:217], v180 offset:0x1000
	s_waitcnt lgkmcnt(3)
	v_mfma_f32_32x32x16_bf16 v[144:159], v[194:197], v[202:205], v[144:159]
	v_mfma_f32_32x32x16_bf16 v[128:143], v[198:201], v[202:205], v[128:143]
	ds_read_b128 v[194:197], v182 offset:0x80
	ds_read_b128 v[198:201], v182 offset:0x2080
	ds_read_b128 v[202:205], v180 offset:0x1400
	s_waitcnt lgkmcnt(3)
	v_mfma_f32_32x32x16_bf16 v[144:159], v[206:209], v[214:217], v[144:159]
	v_mfma_f32_32x32x16_bf16 v[128:143], v[210:213], v[214:217], v[128:143]
	ds_read_b128 v[206:209], v183 offset:0x80
	ds_read_b128 v[210:213], v183 offset:0x2080
	ds_read_b128 v[214:217], v180 offset:0x1800
	s_waitcnt lgkmcnt(3)
	v_mfma_f32_32x32x16_bf16 v[144:159], v[194:197], v[202:205], v[144:159]
	v_mfma_f32_32x32x16_bf16 v[128:143], v[198:201], v[202:205], v[128:143]
	ds_read_b128 v[194:197], v184 offset:0x80
	ds_read_b128 v[198:201], v184 offset:0x2080
	s_waitcnt lgkmcnt(2)
	v_mfma_f32_32x32x16_bf16 v[144:159], v[206:209], v[214:217], v[144:159]
	v_mfma_f32_32x32x16_bf16 v[128:143], v[210:213], v[214:217], v[128:143]
	s_waitcnt lgkmcnt(0)
	v_mfma_f32_32x32x16_bf16 v[144:159], v[194:197], v[166:169], v[144:159]
	v_mfma_f32_32x32x16_bf16 v[128:143], v[198:201], v[166:169], v[128:143]
	s_bitcmp0_b32 s100, 8
	s_cbranch_scc1 .Lstg_a19
	s_waitcnt vmcnt(0)
	s_waitcnt lgkmcnt(0)
	s_barrier

.LBB0_612:
	ds_read_b64_tr_b16 v[144:145], v177 offset:0
	ds_read_b64_tr_b16 v[146:147], v177 offset:0x1000
	ds_read_b64_tr_b16 v[148:149], v177 offset:0x2000
	ds_read_b64_tr_b16 v[150:151], v177 offset:0x3000
	ds_read_b64_tr_b16 v[152:153], v177 offset:0x4000
	ds_read_b64_tr_b16 v[154:155], v177 offset:0x5000
	ds_read_b64_tr_b16 v[156:157], v177 offset:0x6000
	ds_read_b64_tr_b16 v[158:159], v177 offset:0x7000
	s_waitcnt lgkmcnt(6)
	s_nop 0
	v_mfma_f32_32x32x16_bf16 v[112:127], v[144:147], v[128:131], v[112:127]
	ds_read_b64_tr_b16 v[192:193], v177 offset:0x200
	ds_read_b64_tr_b16 v[194:195], v177 offset:0x1200
	s_waitcnt lgkmcnt(6)
	v_mfma_f32_32x32x16_bf16 v[112:127], v[148:151], v[132:135], v[112:127]
	ds_read_b64_tr_b16 v[196:197], v177 offset:0x2200
	ds_read_b64_tr_b16 v[198:199], v177 offset:0x3200
	s_waitcnt lgkmcnt(6)
	v_mfma_f32_32x32x16_bf16 v[112:127], v[152:155], v[136:139], v[112:127]
	ds_read_b64_tr_b16 v[200:201], v177 offset:0x4200
	ds_read_b64_tr_b16 v[202:203], v177 offset:0x5200
	s_waitcnt lgkmcnt(6)
	v_mfma_f32_32x32x16_bf16 v[112:127], v[156:159], v[140:143], v[112:127]
	ds_read_b64_tr_b16 v[204:205], v177 offset:0x6200
	ds_read_b64_tr_b16 v[206:207], v177 offset:0x7200
	s_waitcnt lgkmcnt(6)
	v_mfma_f32_32x32x16_bf16 v[96:111], v[192:195], v[128:131], v[96:111]
	ds_read_b64_tr_b16 v[144:145], v177 offset:0x400
	ds_read_b64_tr_b16 v[146:147], v177 offset:0x1400
	s_waitcnt lgkmcnt(6)
	v_mfma_f32_32x32x16_bf16 v[96:111], v[196:199], v[132:135], v[96:111]
	ds_read_b64_tr_b16 v[148:149], v177 offset:0x2400
	ds_read_b64_tr_b16 v[150:151], v177 offset:0x3400
	s_waitcnt lgkmcnt(6)
	v_mfma_f32_32x32x16_bf16 v[96:111], v[200:203], v[136:139], v[96:111]
	ds_read_b64_tr_b16 v[152:153], v177 offset:0x4400
	ds_read_b64_tr_b16 v[154:155], v177 offset:0x5400
	s_waitcnt lgkmcnt(6)
	v_mfma_f32_32x32x16_bf16 v[96:111], v[204:207], v[140:143], v[96:111]
	ds_read_b64_tr_b16 v[156:157], v177 offset:0x6400
	ds_read_b64_tr_b16 v[158:159], v177 offset:0x7400
	s_waitcnt lgkmcnt(6)
	v_mfma_f32_32x32x16_bf16 v[80:95], v[144:147], v[128:131], v[80:95]
	ds_read_b64_tr_b16 v[192:193], v177 offset:0x600
	ds_read_b64_tr_b16 v[194:195], v177 offset:0x1600
	s_waitcnt lgkmcnt(6)
	v_mfma_f32_32x32x16_bf16 v[80:95], v[148:151], v[132:135], v[80:95]
	ds_read_b64_tr_b16 v[196:197], v177 offset:0x2600
	ds_read_b64_tr_b16 v[198:199], v177 offset:0x3600
	s_waitcnt lgkmcnt(6)
	v_mfma_f32_32x32x16_bf16 v[80:95], v[152:155], v[136:139], v[80:95]
	ds_read_b64_tr_b16 v[200:201], v177 offset:0x4600
	ds_read_b64_tr_b16 v[202:203], v177 offset:0x5600
	s_waitcnt lgkmcnt(6)
	v_mfma_f32_32x32x16_bf16 v[80:95], v[156:159], v[140:143], v[80:95]
	ds_read_b64_tr_b16 v[204:205], v177 offset:0x6600
	ds_read_b64_tr_b16 v[206:207], v177 offset:0x7600
	s_waitcnt lgkmcnt(6)
	v_mfma_f32_32x32x16_bf16 v[64:79], v[192:195], v[128:131], v[64:79]
	ds_read_b64_tr_b16 v[144:145], v177 offset:0x800
	ds_read_b64_tr_b16 v[146:147], v177 offset:0x1800
	s_waitcnt lgkmcnt(6)
	v_mfma_f32_32x32x16_bf16 v[64:79], v[196:199], v[132:135], v[64:79]
	ds_read_b64_tr_b16 v[148:149], v177 offset:0x2800
	ds_read_b64_tr_b16 v[150:151], v177 offset:0x3800
	s_waitcnt lgkmcnt(6)
	v_mfma_f32_32x32x16_bf16 v[64:79], v[200:203], v[136:139], v[64:79]
	ds_read_b64_tr_b16 v[152:153], v177 offset:0x4800
	ds_read_b64_tr_b16 v[154:155], v177 offset:0x5800
	s_waitcnt lgkmcnt(6)
	v_mfma_f32_32x32x16_bf16 v[64:79], v[204:207], v[140:143], v[64:79]
	ds_read_b64_tr_b16 v[156:157], v177 offset:0x6800
	ds_read_b64_tr_b16 v[158:159], v177 offset:0x7800
	s_waitcnt lgkmcnt(6)
	v_mfma_f32_32x32x16_bf16 v[48:63], v[144:147], v[128:131], v[48:63]
	ds_read_b64_tr_b16 v[192:193], v177 offset:0xa00
	ds_read_b64_tr_b16 v[194:195], v177 offset:0x1a00
	s_waitcnt lgkmcnt(6)
	v_mfma_f32_32x32x16_bf16 v[48:63], v[148:151], v[132:135], v[48:63]
	ds_read_b64_tr_b16 v[196:197], v177 offset:0x2a00
	ds_read_b64_tr_b16 v[198:199], v177 offset:0x3a00
	s_waitcnt lgkmcnt(6)
	v_mfma_f32_32x32x16_bf16 v[48:63], v[152:155], v[136:139], v[48:63]
	ds_read_b64_tr_b16 v[200:201], v177 offset:0x4a00
	ds_read_b64_tr_b16 v[202:203], v177 offset:0x5a00
	s_waitcnt lgkmcnt(6)
	v_mfma_f32_32x32x16_bf16 v[48:63], v[156:159], v[140:143], v[48:63]
	ds_read_b64_tr_b16 v[204:205], v177 offset:0x6a00
	ds_read_b64_tr_b16 v[206:207], v177 offset:0x7a00
	s_waitcnt lgkmcnt(6)
	v_mfma_f32_32x32x16_bf16 v[32:47], v[192:195], v[128:131], v[32:47]
	ds_read_b64_tr_b16 v[144:145], v177 offset:0xc00
	ds_read_b64_tr_b16 v[146:147], v177 offset:0x1c00
	s_waitcnt lgkmcnt(6)
	v_mfma_f32_32x32x16_bf16 v[32:47], v[196:199], v[132:135], v[32:47]
	ds_read_b64_tr_b16 v[148:149], v177 offset:0x2c00
	ds_read_b64_tr_b16 v[150:151], v177 offset:0x3c00
	s_waitcnt lgkmcnt(6)
	v_mfma_f32_32x32x16_bf16 v[32:47], v[200:203], v[136:139], v[32:47]
	ds_read_b64_tr_b16 v[152:153], v177 offset:0x4c00
	ds_read_b64_tr_b16 v[154:155], v177 offset:0x5c00
	s_waitcnt lgkmcnt(6)
	v_mfma_f32_32x32x16_bf16 v[32:47], v[204:207], v[140:143], v[32:47]
	ds_read_b64_tr_b16 v[156:157], v177 offset:0x6c00
	ds_read_b64_tr_b16 v[158:159], v177 offset:0x7c00
	s_waitcnt lgkmcnt(6)
	v_mfma_f32_32x32x16_bf16 v[16:31], v[144:147], v[128:131], v[16:31]
	ds_read_b64_tr_b16 v[192:193], v177 offset:0xe00
	ds_read_b64_tr_b16 v[194:195], v177 offset:0x1e00
	s_waitcnt lgkmcnt(6)
	v_mfma_f32_32x32x16_bf16 v[16:31], v[148:151], v[132:135], v[16:31]
	ds_read_b64_tr_b16 v[196:197], v177 offset:0x2e00
	ds_read_b64_tr_b16 v[198:199], v177 offset:0x3e00
	s_waitcnt lgkmcnt(6)
	v_mfma_f32_32x32x16_bf16 v[16:31], v[152:155], v[136:139], v[16:31]
	ds_read_b64_tr_b16 v[200:201], v177 offset:0x4e00
	ds_read_b64_tr_b16 v[202:203], v177 offset:0x5e00
	s_waitcnt lgkmcnt(6)
	v_mfma_f32_32x32x16_bf16 v[16:31], v[156:159], v[140:143], v[16:31]
	ds_read_b64_tr_b16 v[204:205], v177 offset:0x6e00
	ds_read_b64_tr_b16 v[206:207], v177 offset:0x7e00
	s_waitcnt lgkmcnt(6)
	v_mfma_f32_32x32x16_bf16 v[0:15], v[192:195], v[128:131], v[0:15]
	s_waitcnt lgkmcnt(4)
	v_mfma_f32_32x32x16_bf16 v[0:15], v[196:199], v[132:135], v[0:15]
	s_waitcnt lgkmcnt(2)
	v_mfma_f32_32x32x16_bf16 v[0:15], v[200:203], v[136:139], v[0:15]
	s_waitcnt lgkmcnt(0)
	v_mfma_f32_32x32x16_bf16 v[0:15], v[204:207], v[140:143], v[0:15]
	ds_read_b128 v[128:131], v188 offset:0
	ds_read_b128 v[132:135], v188 offset:0x2000
	ds_read_b128 v[136:139], v180 offset:0
	ds_read_b128 v[192:195], v187 offset:0
	ds_read_b128 v[196:199], v187 offset:0x2000
	ds_read_b128 v[200:203], v180 offset:0x400
	s_waitcnt lgkmcnt(3)
	s_nop 0
	v_mfma_f32_32x32x16_bf16 v[144:159], v[128:131], v[136:139], 0
	v_mfma_f32_32x32x16_bf16 v[128:143], v[132:135], v[136:139], 0
	ds_read_b128 v[204:207], v186 offset:0
	ds_read_b128 v[208:211], v186 offset:0x2000
	ds_read_b128 v[212:215], v180 offset:0x800
	s_waitcnt lgkmcnt(3)
	v_mfma_f32_32x32x16_bf16 v[144:159], v[192:195], v[200:203], v[144:159]
	v_mfma_f32_32x32x16_bf16 v[128:143], v[196:199], v[200:203], v[128:143]
	ds_read_b128 v[192:195], v185 offset:0
	ds_read_b128 v[196:199], v185 offset:0x2000
	ds_read_b128 v[200:203], v180 offset:0xc00
	s_waitcnt lgkmcnt(3)
	v_mfma_f32_32x32x16_bf16 v[144:159], v[204:207], v[212:215], v[144:159]
	v_mfma_f32_32x32x16_bf16 v[128:143], v[208:211], v[212:215], v[128:143]
	ds_read_b128 v[204:207], v188 offset:0x80
	ds_read_b128 v[208:211], v188 offset:0x2080
	ds_read_b128 v[212:215], v180 offset:0x1000
	s_waitcnt lgkmcnt(3)
	v_mfma_f32_32x32x16_bf16 v[144:159], v[192:195], v[200:203], v[144:159]
	v_mfma_f32_32x32x16_bf16 v[128:143], v[196:199], v[200:203], v[128:143]
	ds_read_b128 v[192:195], v187 offset:0x80
	ds_read_b128 v[196:199], v187 offset:0x2080
	ds_read_b128 v[200:203], v180 offset:0x1400
	s_waitcnt lgkmcnt(3)
	v_mfma_f32_32x32x16_bf16 v[144:159], v[204:207], v[212:215], v[144:159]
	v_mfma_f32_32x32x16_bf16 v[128:143], v[208:211], v[212:215], v[128:143]
	ds_read_b128 v[204:207], v186 offset:0x80
	ds_read_b128 v[208:211], v186 offset:0x2080
	ds_read_b128 v[186:189], v180 offset:0x1800
	s_waitcnt lgkmcnt(3)
	v_mfma_f32_32x32x16_bf16 v[144:159], v[192:195], v[200:203], v[144:159]
	v_mfma_f32_32x32x16_bf16 v[128:143], v[196:199], v[200:203], v[128:143]
	ds_read_b128 v[180:183], v185 offset:0x80
	ds_read_b128 v[192:195], v185 offset:0x2080
	s_waitcnt lgkmcnt(2)
	v_mfma_f32_32x32x16_bf16 v[144:159], v[204:207], v[186:189], v[144:159]
	v_mfma_f32_32x32x16_bf16 v[128:143], v[208:211], v[186:189], v[128:143]
	s_waitcnt lgkmcnt(0)
	v_mfma_f32_32x32x16_bf16 v[144:159], v[180:183], v[166:169], v[144:159]
	v_mfma_f32_32x32x16_bf16 v[128:143], v[192:195], v[166:169], v[128:143]
	s_bitcmp0_b32 s100, 8
	s_cbranch_scc1 .Lstg_a20
	s_waitcnt vmcnt(0)
	s_waitcnt lgkmcnt(0)
	s_barrier
